# ffn_act (both variants): all U row loads issued up front through SGPR-base addressing, 64-bit address chains removed, waits recomputed; attention layer 3 same tile-loop changes as layers 0-2
# baseline (speedup 1.0000x reference)
.LBB0_1276:
	v_readlane_b32 s0, v251, 54
	v_readlane_b32 s1, v251, 55
	s_andn2_b64 vcc, exec, s[0:1]
	v_readfirstlane_b32 s0, v219
	s_waitcnt lgkmcnt(0)
	s_barrier
	s_cbranch_vccnz .LBB0_1292
	v_lshrrev_b32_e32 v0, 2, v219
	v_and_or_b32 v0, v0, 4, v167
	s_ashr_i32 s6, s0, 6
	v_lshlrev_b32_e32 v3, 1, v0
	v_or_b32_e32 v0, v170, v167
	s_lshl_b32 s7, s6, 3
	v_lshlrev_b32_e32 v0, 8, v0
	s_waitcnt vmcnt(14)
	v_and_b32_e32 v4, 8, v220
	v_lshrrev_b32_e32 v1, 4, v219
	v_add3_u32 v220, 0, v0, v4
	v_bitop3_b32 v0, s7, v219, v159 bitop3:0x36
	v_mov_b32_e32 v171, v33
	v_lshlrev_b32_e32 v0, 3, v0
	v_bitop3_b32 v1, v1, v166, 3 bitop3:0x6c
	s_and_b32 s10, s0, 0xffffff80
	s_lshl_b32 s0, s6, 5
	v_or_b32_e32 v2, s7, v159
	v_lshl_add_u64 v[172:173], s[4:5], 0, v[170:171]
	v_and_b32_e32 v176, 0x78, v0
	v_lshlrev_b32_e32 v0, 3, v166
	v_lshlrev_b32_e32 v4, 4, v159
	v_lshlrev_b32_e32 v171, 4, v1
	v_bitop3_b32 v1, v159, v166, 4 bitop3:0x36
	v_and_or_b32 v177, s0, 32, v166
	v_bfe_u32 v5, v219, 1, 1
	v_mad_i64_i32 v[174:175], s[0:1], v2, s96, 0
	v_xor_b32_e32 v0, v4, v0
	v_or_b32_e32 v4, 4, v2
	v_bitop3_b32 v2, v2, v219, 4 bitop3:0x36
	v_lshlrev_b32_e32 v219, 4, v1
	v_bitop3_b32 v1, v159, v166, 8 bitop3:0x36
	v_lshlrev_b32_e32 v222, 4, v1
	v_bitop3_b32 v1, v159, v166, 12 bitop3:0x36
	v_lshlrev_b32_e32 v223, 4, v1
	v_or_b32_e32 v1, v3, v5
	v_lshlrev_b32_e32 v224, 4, v1
	v_bitop3_b32 v1, v3, v5, 2 bitop3:0x1e
	v_lshlrev_b32_e32 v225, 4, v1
	v_bitop3_b32 v1, v3, v5, 4 bitop3:0x1e
	v_mad_i64_i32 v[178:179], s[0:1], v4, s96, 0
	v_lshlrev_b32_e32 v237, 4, v1
	v_bitop3_b32 v1, v3, v5, 6 bitop3:0x1e
	v_lshlrev_b32_e32 v238, 4, v1
	v_bitop3_b32 v1, v3, v5, 8 bitop3:0x1e
	s_lshl_b32 s0, s6, 14
	v_lshlrev_b32_e32 v4, 1, v4
	v_lshlrev_b32_e32 v239, 4, v1
	v_bitop3_b32 v1, v3, v5, 10 bitop3:0x1e
	s_and_b32 s0, s0, 0x4000
	v_lshlrev_b32_e32 v2, 3, v2
	v_bitop3_b32 v4, v4, v166, 14 bitop3:0x6c
	v_lshlrev_b32_e32 v240, 4, v1
	v_bitop3_b32 v1, v3, v5, 12 bitop3:0x1e
	s_add_i32 s0, s0, 0
	s_lshl_b32 s8, s6, 11
	v_and_b32_e32 v2, 0x78, v2
	v_lshlrev_b32_e32 v4, 3, v4
	v_add_u32_e32 v180, 0x2000, v168
	v_add_u32_e32 v182, 0x4000, v168
	v_add_u32_e32 v184, 0x6000, v168
	v_lshlrev_b32_e32 v241, 4, v1
	v_bitop3_b32 v1, v3, v5, 14 bitop3:0x1e
	s_add_i32 s0, s0, 0x10000
	s_addk_i32 s7, 0x44
	v_lshl_add_u32 v221, v166, 8, 0
	s_add_i32 s11, s8, 0
	v_ashrrev_i32_e32 v169, 31, v168
	v_ashrrev_i32_e32 v181, 31, v180
	v_ashrrev_i32_e32 v183, 31, v182
	v_ashrrev_i32_e32 v185, 31, v184
	v_lshlrev_b32_e32 v242, 4, v1
	v_lshl_add_u32 v243, v166, 9, s0
	v_or_b32_e32 v244, s7, v159
	v_lshlrev_b32_e32 v166, 1, v0
	v_lshlrev_b32_e32 v186, 1, v2
	v_lshlrev_b32_e32 v188, 1, v4
	v_add3_u32 v166, v174, v166, s90
	v_add3_u32 v186, v178, v186, s84
	v_add3_u32 v188, v178, v188, s90
	v_lshlrev_b32_e32 v190, 1, v158
	s_mov_b32 s12, s83
	s_branch .LBB0_1279

.LBB0_1279:
	s_and_b32 s0, s12, 3
	s_lshl_b32 s1, s12, 10
	s_and_b32 s15, s1, 0x1000
	s_lshl_b32 s1, s0, 9
	s_ashr_i32 s13, s12, 3
	s_add_i32 s4, s1, s10
	s_sub_i32 s14, 63, s13
	s_ashr_i32 s5, s4, 31
	s_mul_i32 s1, s15, 0x9000
	s_add_u32 s1, s2, s1
	s_addc_u32 s6, s3, 0
	s_lshl_b32 s0, s0, 8
	s_add_u32 s0, s1, s0
	s_addc_u32 s1, s6, 0
	v_lshlrev_b32_e32 v32, 1, v176
	v_lshl_add_u64 v[192:193], v[172:173], 0, s[4:5]
	v_add3_u32 v32, v174, v32, s84
	s_mov_b64 s[6:7], -1
	s_lshl_b64 s[4:5], s[4:5], 1
	s_branch .LBB0_1281

.LBB0_1281:
	s_and_b64 s[8:9], s[6:7], exec
	s_cselect_b32 s16, s13, s14
	s_lshl_b32 s8, s16, 6
	s_add_i32 s8, s8, s15
	v_or_b32_e32 v214, s8, v177
	v_mov_b64_e32 v[0:1], s[2:3]
	v_mad_i64_i32 v[2:3], s[18:19], v214, s96, v[0:1]
	v_lshl_add_u64 v[2:3], v[2:3], 0, s[4:5]
	v_mov_b32_e32 v191, v33
	v_or_b32_e32 v212, 16, v214
	v_lshl_add_u64 v[2:3], v[2:3], 0, v[190:191]
	s_mov_b64 s[20:21], 0x5000
	v_mad_i64_i32 v[0:1], s[18:19], v212, s96, v[0:1]
	v_lshl_add_u64 v[4:5], v[2:3], 0, s[20:21]
	v_add_co_u32_e32 v2, vcc, 0x5000, v2
	v_lshl_add_u64 v[0:1], v[0:1], 0, s[4:5]
	s_nop 0
	v_addc_co_u32_e32 v3, vcc, 0, v3, vcc
	v_lshl_add_u64 v[0:1], v[0:1], 0, v[190:191]
	s_mov_b32 m0, s11
	global_load_dwordx4 v[70:73], v[4:5], off offset:64
	global_load_dwordx4 v[74:77], v[4:5], off offset:128
	global_load_dwordx4 v[78:81], v[2:3], off
	global_load_dwordx4 v[82:85], v[4:5], off offset:192
	v_lshl_add_u64 v[2:3], v[0:1], 0, s[20:21]
	v_add_co_u32_e32 v0, vcc, 0x5000, v0
	s_ashr_i32 s9, s8, 31
	s_nop 0
	v_addc_co_u32_e32 v1, vcc, 0, v1, vcc
	global_load_dwordx4 v[86:89], v[2:3], off offset:64
	global_load_dwordx4 v[90:93], v[2:3], off offset:128
	global_load_dwordx4 v[94:97], v[0:1], off
	global_load_dwordx4 v[98:101], v[2:3], off offset:192
	s_barrier
	global_load_lds_dwordx4 v32, s[0:1]
	s_add_i32 m0, s11, 0x8000
	s_lshl_b64 s[8:9], s[8:9], 9
	global_load_lds_dwordx4 v166, s[0:1]
	s_add_i32 m0, s11, 0x400
	s_waitcnt vmcnt(0)
	v_add_u32_e32 v24, 0, v168
	global_load_lds_dwordx4 v186, s[0:1]
	s_add_i32 m0, s11, 0x8400
	s_add_u32 s100, s0, 0x240000
	s_addc_u32 s101, s1, 0
	s_add_u32 s8, s24, s8
	s_addc_u32 s9, s25, s9
	v_lshl_add_u64 v[0:1], s[8:9], 0, v[168:169]
	v_lshl_add_u64 v[2:3], s[8:9], 0, v[180:181]
	global_load_dwordx4 v[28:31], v[0:1], off
	global_load_dwordx4 v[38:41], v[2:3], off
	v_lshl_add_u64 v[0:1], s[8:9], 0, v[182:183]
	v_lshl_add_u64 v[2:3], s[8:9], 0, v[184:185]
	global_load_dwordx4 v[42:45], v[0:1], off
	global_load_dwordx4 v[46:49], v[2:3], off
	v_add_u32_e32 v24, 0x10000, v24
	global_load_lds_dwordx4 v188, s[0:1]
	v_mov_b32_e32 v3, 0
	v_mov_b32_e32 v2, 0
	v_mov_b32_e32 v1, 0
	v_mov_b32_e32 v0, 0
	v_mov_b32_e32 v7, 0
	v_mov_b32_e32 v6, 0
	v_mov_b32_e32 v5, 0
	v_mov_b32_e32 v4, 0
	v_mov_b32_e32 v11, 0
	v_mov_b32_e32 v10, 0
	v_mov_b32_e32 v9, 0
	v_mov_b32_e32 v8, 0
	v_mov_b32_e32 v15, 0
	v_mov_b32_e32 v14, 0
	v_mov_b32_e32 v13, 0
	v_mov_b32_e32 v12, 0
	v_mov_b32_e32 v19, 0
	v_mov_b32_e32 v18, 0
	v_mov_b32_e32 v17, 0
	v_mov_b32_e32 v16, 0
	v_mov_b32_e32 v23, 0
	v_mov_b32_e32 v22, 0
	v_mov_b32_e32 v21, 0
	v_mov_b32_e32 v20, 0
	v_mov_b32_e32 v27, 0
	s_cmp_lt_i32 s16, 0
	v_mov_b32_e32 v26, 0
	v_mov_b32_e32 v25, 0
	v_mov_b32_e32 v53, 0
	v_mov_b32_e32 v52, 0
	v_mov_b32_e32 v51, 0
	v_mov_b32_e32 v50, 0
	v_mov_b32_e32 v57, 0
	v_mov_b32_e32 v56, 0
	v_mov_b32_e32 v55, 0
	v_mov_b32_e32 v54, 0
	v_mov_b32_e32 v61, 0
	v_mov_b32_e32 v60, 0
	v_mov_b32_e32 v59, 0
	v_mov_b32_e32 v58, 0
	v_mov_b32_e32 v65, 0
	v_mov_b32_e32 v64, 0
	s_waitcnt vmcnt(0)
	ds_write_b128 v24, v[28:31]
	ds_write_b128 v24, v[38:41] offset:8192
	ds_write_b128 v24, v[42:45] offset:16384
	ds_write_b128 v24, v[46:49] offset:24576
	s_waitcnt vmcnt(0)
	v_mov_b32_e32 v24, 0
	v_mov_b32_e32 v31, 0
	v_mov_b32_e32 v30, 0
	v_mov_b32_e32 v29, 0
	v_mov_b32_e32 v28, 0
	v_mov_b32_e32 v45, 0
	v_mov_b32_e32 v44, 0
	v_mov_b32_e32 v43, 0
	v_mov_b32_e32 v42, 0
	v_mov_b32_e32 v41, 0
	v_mov_b32_e32 v40, 0
	v_mov_b32_e32 v39, 0
	v_mov_b32_e32 v38, 0
	v_mov_b32_e32 v49, 0
	v_mov_b32_e32 v48, 0
	v_mov_b32_e32 v47, 0
	v_mov_b32_e32 v46, 0
	v_mov_b32_e32 v63, 0
	v_mov_b32_e32 v62, 0
	v_mov_b32_e32 v69, 0
	v_mov_b32_e32 v68, 0
	v_mov_b32_e32 v67, 0
	v_mov_b32_e32 v66, 0
	v_mov_b32_e32 v102, 0
	v_mov_b32_e32 v103, 0
	s_waitcnt lgkmcnt(0)
	s_barrier
	s_cbranch_scc1 .LBB0_1280
	v_mov_b32_e32 v66, v33
	v_mov_b32_e32 v67, v33
	v_mov_b32_e32 v68, v33
	v_mov_b32_e32 v69, v33
	v_mov_b64_e32 v[62:63], v[66:67]
	v_mov_b64_e32 v[58:59], v[66:67]
	v_mov_b64_e32 v[54:55], v[66:67]
	v_mov_b64_e32 v[50:51], v[66:67]
	v_mov_b64_e32 v[46:47], v[66:67]
	v_mov_b64_e32 v[38:39], v[66:67]
	v_mov_b64_e32 v[42:43], v[66:67]
	v_mov_b64_e32 v[28:29], v[66:67]
	v_mov_b64_e32 v[24:25], v[66:67]
	v_mov_b64_e32 v[20:21], v[66:67]
	v_mov_b64_e32 v[16:17], v[66:67]
	v_mov_b64_e32 v[12:13], v[66:67]
	v_mov_b64_e32 v[8:9], v[66:67]
	v_mov_b64_e32 v[4:5], v[66:67]
	v_mov_b64_e32 v[0:1], v[66:67]
	s_add_i32 s17, s16, 1
	s_mov_b32 s18, 0
	v_mov_b32_e32 v246, 0xf149f2ca
	v_mov_b32_e32 v215, 0
	v_mov_b32_e32 v213, v243
	v_mov_b32_e32 v245, 0
	v_mov_b32_e32 v218, 0xf149f2ca
	v_mov_b64_e32 v[64:65], v[68:69]
	v_mov_b64_e32 v[60:61], v[68:69]
	v_mov_b64_e32 v[56:57], v[68:69]
	v_mov_b64_e32 v[52:53], v[68:69]
	v_mov_b64_e32 v[48:49], v[68:69]
	v_mov_b64_e32 v[40:41], v[68:69]
	v_mov_b64_e32 v[44:45], v[68:69]
	v_mov_b64_e32 v[30:31], v[68:69]
	v_mov_b64_e32 v[26:27], v[68:69]
	v_mov_b64_e32 v[22:23], v[68:69]
	v_mov_b64_e32 v[18:19], v[68:69]
	v_mov_b64_e32 v[14:15], v[68:69]
	v_mov_b64_e32 v[10:11], v[68:69]
	v_mov_b64_e32 v[6:7], v[68:69]
	v_mov_b64_e32 v[2:3], v[68:69]
	s_and_b32 s20, s18, 1
	s_cmp_lt_i32 s18, s16
	s_mov_b64 s[8:9], -1
	s_cbranch_scc1 .LBB0_1285
	s_branch .LBB0_1284
.LBB0_1283:
	v_mov_b32_e32 v246, v189
	v_mov_b32_e32 v218, v247
	s_and_b32 s20, s18, 1
	s_cmp_lt_i32 s18, s16
	s_mov_b64 s[8:9], -1
	s_cbranch_scc1 .LBB0_1285

.LBB0_1285:
	s_andn2_b64 vcc, exec, s[8:9]
	s_cbranch_vccnz .LBB0_1287
	s_lshl_b32 s19, s20, 14
	s_xor_b32 s20, s19, 0x4000
	s_add_i32 s20, s11, s20
	s_mov_b32 m0, s20
	s_nop 0
	global_load_lds_dwordx4 v32, s[100:101]
	s_add_i32 m0, s20, 0x8000
	s_nop 0
	global_load_lds_dwordx4 v166, s[100:101]
	s_add_i32 m0, s20, 0x400
	s_nop 0
	global_load_lds_dwordx4 v186, s[100:101]
	s_add_i32 m0, s20, 0x8400
	s_nop 0
	global_load_lds_dwordx4 v188, s[100:101]
	s_add_u32 s100, s100, 0x240000
	s_addc_u32 s101, s101, 0
.LBB0_1287:
	v_add_u32_e32 v114, s19, v221
	v_add_u32_e32 v142, v114, v171
	ds_read_b128 v[102:105], v142
	v_add_u32_e32 v143, v114, v219
	ds_read_b128 v[106:109], v143
	v_add_u32_e32 v144, v114, v222
	ds_read_b128 v[110:113], v144
	v_add_u32_e32 v145, v114, v223
	ds_read_b128 v[114:117], v145
	ds_read_b128 v[118:121], v142 offset:4096
	ds_read_b128 v[122:125], v143 offset:4096
	ds_read_b128 v[126:129], v144 offset:4096
	ds_read_b128 v[130:133], v145 offset:4096
	s_waitcnt lgkmcnt(0)
	v_mfma_f32_16x16x32_bf16 v[138:141], v[118:121], v[78:81], 0
	v_add_u32_e32 v187, s19, v220
	v_mfma_f32_16x16x32_bf16 v[134:137], v[102:105], v[78:81], 0
	v_mfma_f32_16x16x32_bf16 v[102:105], v[102:105], v[94:97], 0
	v_mfma_f32_16x16x32_bf16 v[118:121], v[118:121], v[94:97], 0
	v_mfma_f32_16x16x32_bf16 v[134:137], v[106:109], v[70:73], v[134:137]
	v_mfma_f32_16x16x32_bf16 v[102:105], v[106:109], v[86:89], v[102:105]
	v_mfma_f32_16x16x32_bf16 v[138:141], v[122:125], v[70:73], v[138:141]
	v_mfma_f32_16x16x32_bf16 v[118:121], v[122:125], v[86:89], v[118:121]
	v_mfma_f32_16x16x32_bf16 v[134:137], v[110:113], v[74:77], v[134:137]
	v_mfma_f32_16x16x32_bf16 v[102:105], v[110:113], v[90:93], v[102:105]
	v_mfma_f32_16x16x32_bf16 v[138:141], v[126:129], v[74:77], v[138:141]
	v_mfma_f32_16x16x32_bf16 v[118:121], v[126:129], v[90:93], v[118:121]
	v_mfma_f32_16x16x32_bf16 v[162:165], v[114:117], v[82:85], v[134:137]
	v_mfma_f32_16x16x32_bf16 v[134:137], v[114:117], v[98:101], v[102:105]
	s_nop 3
	ds_read_b128 v[102:105], v142 offset:8192
	ds_read_b128 v[106:109], v143 offset:8192
	ds_read_b128 v[110:113], v144 offset:8192
	ds_read_b128 v[114:117], v145 offset:8192
	v_max_f32_e32 v167, v164, v165
	v_mfma_f32_16x16x32_bf16 v[158:161], v[130:133], v[82:85], v[138:141]
	v_max3_f32 v167, v162, v163, v167
	v_mfma_f32_16x16x32_bf16 v[138:141], v[130:133], v[98:101], v[118:121]
	s_nop 2
	ds_read_b128 v[118:121], v142 offset:12288
	ds_read_b128 v[122:125], v143 offset:12288
	ds_read_b128 v[126:129], v144 offset:12288
	ds_read_b128 v[130:133], v145 offset:12288
	v_max3_f32 v189, v159, v160, v161
	v_max3_f32 v167, v167, v158, v189
	s_waitcnt lgkmcnt(0)
	v_mfma_f32_16x16x32_bf16 v[142:145], v[102:105], v[78:81], 0
	v_mfma_f32_16x16x32_bf16 v[102:105], v[102:105], v[94:97], 0
	v_mfma_f32_16x16x32_bf16 v[102:105], v[106:109], v[86:89], v[102:105]
	v_mfma_f32_16x16x32_bf16 v[102:105], v[110:113], v[90:93], v[102:105]
	v_mfma_f32_16x16x32_bf16 v[146:149], v[114:117], v[98:101], v[102:105]
	v_mfma_f32_16x16x32_bf16 v[102:105], v[118:121], v[78:81], 0
	v_mfma_f32_16x16x32_bf16 v[142:145], v[106:109], v[70:73], v[142:145]
	v_mfma_f32_16x16x32_bf16 v[102:105], v[122:125], v[70:73], v[102:105]
	v_mfma_f32_16x16x32_bf16 v[142:145], v[110:113], v[74:77], v[142:145]
	v_mfma_f32_16x16x32_bf16 v[102:105], v[126:129], v[74:77], v[102:105]
	v_mfma_f32_16x16x32_bf16 v[154:157], v[114:117], v[82:85], v[142:145]
	v_mfma_f32_16x16x32_bf16 v[150:153], v[130:133], v[82:85], v[102:105]
	v_mfma_f32_16x16x32_bf16 v[102:105], v[118:121], v[94:97], 0
	s_nop 5
	v_max3_f32 v189, v155, v156, v157
	v_max3_f32 v167, v167, v154, v189
	v_max3_f32 v189, v151, v152, v153
	v_mfma_f32_16x16x32_bf16 v[102:105], v[122:125], v[86:89], v[102:105]
	v_max3_f32 v167, v167, v150, v189
	v_mov_b32_e32 v189, v167
	s_nop 1
	v_permlane16_swap_b32_e32 v167, v189
	v_mfma_f32_16x16x32_bf16 v[102:105], v[126:129], v[90:93], v[102:105]
	v_max_f32 v167, v167, v189
	s_nop 0
	v_mov_b32_e32 v189, v167
	s_nop 1
	v_permlane32_swap_b32_e32 v167, v189
	v_max_f32 v167, v167, v189
	v_mfma_f32_16x16x32_bf16 v[142:145], v[130:133], v[98:101], v[102:105]
	v_mul_f32_e32 v167, 0x3e0293ee, v167
	v_add_f32_e32 v189, 0x41000000, v246
	v_cmp_gt_f32_e32 vcc, v167, v189
	v_add_u32_e32 v102, v187, v224
	ds_read_b64_tr_b16 v[130:131], v102 offset:32768
	ds_read_b64_tr_b16 v[132:133], v102 offset:36864
	ds_read_b64_tr_b16 v[122:123], v102 offset:40960
	ds_read_b64_tr_b16 v[124:125], v102 offset:45056
	v_add_u32_e32 v102, v187, v225
	ds_read_b64_tr_b16 v[126:127], v102 offset:32768
	ds_read_b64_tr_b16 v[128:129], v102 offset:36864
	ds_read_b64_tr_b16 v[114:115], v102 offset:40960
	ds_read_b64_tr_b16 v[116:117], v102 offset:45056
	v_add_u32_e32 v102, v187, v237
	v_add_u32_e32 v104, v187, v238
	v_cndmask_b32_e32 v189, v246, v167, vcc
	ds_read_b64_tr_b16 v[118:119], v102 offset:32768
	ds_read_b64_tr_b16 v[120:121], v102 offset:36864
	ds_read_b64_tr_b16 v[110:111], v102 offset:40960
	ds_read_b64_tr_b16 v[112:113], v102 offset:45056
	ds_read_b64_tr_b16 v[106:107], v104 offset:32768
	ds_read_b64_tr_b16 v[108:109], v104 offset:36864
	ds_read_b64_tr_b16 v[102:103], v104 offset:40960
	ds_read_b64_tr_b16 v[104:105], v104 offset:45056
	ds_read_b64 v[198:199], v213
	v_fma_f32 v162, v162, s97, -v189
	v_exp_f32_e32 v162, v162
	v_fma_f32 v163, v163, s97, -v189
	v_exp_f32_e32 v163, v163
	v_fma_f32 v164, v164, s97, -v189
	v_exp_f32_e32 v164, v164
	v_fma_f32 v165, v165, s97, -v189
	v_exp_f32_e32 v165, v165
	v_fma_f32 v158, v158, s97, -v189
	s_waitcnt lgkmcnt(0)
	v_lshrrev_b64 v[216:217], v170, v[198:199]
	v_bfe_i32 v198, v216, 0, 1
	v_exp_f32_e32 v158, v158
	v_and_b32_e32 v162, v198, v162
	v_fma_f32 v159, v159, s97, -v189
	v_bfe_i32 v199, v216, 1, 1
	v_and_b32_e32 v163, v199, v163
	v_exp_f32_e32 v159, v159
	v_fma_f32 v160, v160, s97, -v189
	v_add_f32_e32 v198, v162, v163
	v_bfe_i32 v199, v216, 2, 1
	v_exp_f32_e32 v160, v160
	v_and_b32_e32 v164, v199, v164
	v_fma_f32 v161, v161, s97, -v189
	v_bfe_i32 v200, v216, 3, 1
	v_add_f32_e32 v198, v198, v164
	v_and_b32_e32 v165, v200, v165
	v_exp_f32_e32 v161, v161
	v_fma_f32 v154, v154, s97, -v189
	v_add_f32_e32 v198, v198, v165
	v_bfe_i32 v199, v216, 16, 1
	v_exp_f32_e32 v154, v154
	v_and_b32_e32 v158, v199, v158
	v_fma_f32 v155, v155, s97, -v189
	v_bfe_i32 v200, v216, 17, 1
	v_add_f32_e32 v198, v198, v158
	v_and_b32_e32 v159, v200, v159
	v_exp_f32_e32 v155, v155
	v_fma_f32 v156, v156, s97, -v189
	v_add_f32_e32 v198, v198, v159
	v_bfe_i32 v199, v216, 18, 1
	v_exp_f32_e32 v156, v156
	v_and_b32_e32 v160, v199, v160
	v_fma_f32 v157, v157, s97, -v189
	v_bfe_i32 v200, v216, 19, 1
	v_add_f32_e32 v198, v198, v160
	v_and_b32_e32 v161, v200, v161
	v_exp_f32_e32 v157, v157
	v_add_f32_e32 v198, v198, v161
	v_bfe_i32 v199, v217, 0, 1
	v_fma_f32 v150, v150, s97, -v189
	v_and_b32_e32 v154, v199, v154
	v_bfe_i32 v200, v217, 1, 1
	v_add_f32_e32 v198, v198, v154
	v_and_b32_e32 v155, v200, v155
	v_exp_f32_e32 v150, v150
	v_fma_f32 v151, v151, s97, -v189
	v_add_f32_e32 v198, v198, v155
	v_bfe_i32 v199, v217, 2, 1
	v_exp_f32_e32 v151, v151
	v_and_b32_e32 v216, v199, v156
	v_fma_f32 v152, v152, s97, -v189
	v_bfe_i32 v200, v217, 3, 1
	v_add_f32_e32 v156, v198, v216
	v_and_b32_e32 v157, v200, v157
	v_exp_f32_e32 v152, v152
	v_fma_f32 v153, v153, s97, -v189
	v_add_f32_e32 v198, v156, v157
	v_bfe_i32 v156, v217, 16, 1
	v_exp_f32_e32 v153, v153
	v_and_b32_e32 v156, v156, v150
	v_bfe_i32 v199, v217, 17, 1
	v_add_f32_e32 v150, v198, v156
	v_and_b32_e32 v151, v199, v151
	v_add_f32_e32 v150, v150, v151
	v_bfe_i32 v198, v217, 18, 1
	v_sub_f32_e32 v167, v246, v189
	v_and_b32_e32 v152, v198, v152
	v_bfe_i32 v199, v217, 19, 1
	v_add_f32_e32 v150, v150, v152
	v_and_b32_e32 v153, v199, v153
	v_add_f32_e32 v198, v150, v153
	v_exp_f32_e32 v150, v167
	s_nop 0
	v_cmp_eq_f32_e32 vcc, 1.0, v150
	v_fma_f32 v215, v215, v150, v198
	s_cmp_eq_u64 vcc, exec
	s_cbranch_scc1 .LBB0_1289
	v_pk_mul_f32 v[68:69], v[68:69], v[150:151] op_sel_hi:[1,0]
	v_pk_mul_f32 v[66:67], v[66:67], v[150:151] op_sel_hi:[1,0]
	v_pk_mul_f32 v[64:65], v[64:65], v[150:151] op_sel_hi:[1,0]
	v_pk_mul_f32 v[62:63], v[62:63], v[150:151] op_sel_hi:[1,0]
	v_pk_mul_f32 v[60:61], v[60:61], v[150:151] op_sel_hi:[1,0]
	v_pk_mul_f32 v[58:59], v[58:59], v[150:151] op_sel_hi:[1,0]
	v_pk_mul_f32 v[56:57], v[56:57], v[150:151] op_sel_hi:[1,0]
	v_pk_mul_f32 v[54:55], v[54:55], v[150:151] op_sel_hi:[1,0]
	v_pk_mul_f32 v[52:53], v[52:53], v[150:151] op_sel_hi:[1,0]
	v_pk_mul_f32 v[50:51], v[50:51], v[150:151] op_sel_hi:[1,0]
	v_pk_mul_f32 v[48:49], v[48:49], v[150:151] op_sel_hi:[1,0]
	v_pk_mul_f32 v[46:47], v[46:47], v[150:151] op_sel_hi:[1,0]
	v_pk_mul_f32 v[40:41], v[40:41], v[150:151] op_sel_hi:[1,0]
	v_pk_mul_f32 v[38:39], v[38:39], v[150:151] op_sel_hi:[1,0]
	v_pk_mul_f32 v[44:45], v[44:45], v[150:151] op_sel_hi:[1,0]
	v_pk_mul_f32 v[42:43], v[42:43], v[150:151] op_sel_hi:[1,0]
.LBB0_1289:
	v_max_f32_e32 v167, v136, v137
	v_max3_f32 v167, v134, v135, v167
	v_max3_f32 v200, v139, v140, v141
	v_max3_f32 v167, v167, v138, v200
	v_max3_f32 v200, v147, v148, v149
	v_max3_f32 v167, v167, v146, v200
	v_max3_f32 v200, v143, v144, v145
	v_max3_f32 v167, v167, v142, v200
	v_mov_b32_e32 v200, v167
	s_nop 1
	v_permlane16_swap_b32_e32 v167, v200
	v_max_f32 v167, v167, v200
	ds_read_b64 v[198:199], v213 offset:8192
	v_mov_b32_e32 v200, v167
	s_nop 1
	v_permlane32_swap_b32_e32 v167, v200
	v_max_f32 v167, v167, v200
	v_add_f32_e32 v200, 0x41000000, v218
	v_mul_f32_e32 v167, 0x3e0293ee, v167
	v_cmp_gt_f32_e32 vcc, v167, v200
	s_waitcnt lgkmcnt(0)
	v_lshrrev_b64 v[198:199], v170, v[198:199]
	v_bfe_i32 v201, v198, 0, 1
	v_cndmask_b32_e32 v247, v218, v167, vcc
	v_fma_f32 v135, v135, s97, -v247
	v_exp_f32_e32 v135, v135
	v_bfe_i32 v167, v198, 1, 1
	v_fma_f32 v134, v134, s97, -v247
	v_exp_f32_e32 v134, v134
	v_and_b32_e32 v167, v167, v135
	v_fma_f32 v135, v136, s97, -v247
	v_fma_f32 v136, v137, s97, -v247
	v_exp_f32_e32 v136, v136
	v_exp_f32_e32 v137, v135
	v_bfe_i32 v135, v198, 3, 1
	v_sub_f32_e32 v200, v218, v247
	v_and_b32_e32 v218, v201, v134
	v_bfe_i32 v201, v198, 2, 1
	v_and_b32_e32 v135, v135, v136
	v_and_b32_e32 v136, v201, v137
	v_fma_f32 v137, v138, s97, -v247
	v_fma_f32 v138, v139, s97, -v247
	v_exp_f32_e32 v138, v138
	v_exp_f32_e32 v139, v137
	v_bfe_i32 v137, v198, 17, 1
	v_bfe_i32 v201, v198, 16, 1
	v_and_b32_e32 v137, v137, v138
	v_and_b32_e32 v138, v201, v139
	v_fma_f32 v139, v140, s97, -v247
	v_fma_f32 v140, v141, s97, -v247
	v_exp_f32_e32 v140, v140
	v_exp_f32_e32 v141, v139
	v_bfe_i32 v139, v198, 19, 1
	v_bfe_i32 v201, v198, 18, 1
	v_add_f32_e32 v134, v218, v167
	v_and_b32_e32 v139, v139, v140
	v_and_b32_e32 v140, v201, v141
	v_fma_f32 v141, v146, s97, -v247
	v_fma_f32 v146, v147, s97, -v247
	v_exp_f32_e32 v146, v146
	v_exp_f32_e32 v147, v141
	v_add_f32_e32 v134, v134, v136
	v_add_f32_e32 v134, v134, v135
	v_bfe_i32 v141, v199, 1, 1
	v_add_f32_e32 v134, v134, v138
	v_bfe_i32 v198, v199, 0, 1
	v_and_b32_e32 v141, v141, v146
	v_and_b32_e32 v146, v198, v147
	v_fma_f32 v147, v148, s97, -v247
	v_fma_f32 v148, v149, s97, -v247
	v_add_f32_e32 v134, v134, v137
	v_exp_f32_e32 v148, v148
	v_exp_f32_e32 v149, v147
	v_add_f32_e32 v134, v134, v140
	v_fma_f32 v142, v142, s97, -v247
	v_add_f32_e32 v134, v134, v139
	v_fma_f32 v143, v143, s97, -v247
	v_exp_f32_e32 v142, v142
	v_add_f32_e32 v134, v134, v146
	v_bfe_i32 v147, v199, 3, 1
	v_exp_f32_e32 v143, v143
	v_fma_f32 v144, v144, s97, -v247
	v_add_f32_e32 v134, v134, v141
	v_bfe_i32 v198, v199, 2, 1
	v_and_b32_e32 v147, v147, v148
	v_and_b32_e32 v148, v198, v149
	v_fma_f32 v145, v145, s97, -v247
	v_exp_f32_e32 v144, v144
	v_add_f32_e32 v134, v134, v148
	v_exp_f32_e32 v145, v145
	v_add_f32_e32 v134, v134, v147
	v_bfe_i32 v149, v199, 16, 1
	v_bfe_i32 v198, v199, 17, 1
	s_nop 0
	v_and_b32_e32 v142, v149, v142
	v_and_b32_e32 v143, v198, v143
	v_add_f32_e32 v134, v134, v142
	v_add_f32_e32 v134, v134, v143
	v_bfe_i32 v149, v199, 18, 1
	v_bfe_i32 v198, v199, 19, 1
	s_nop 0
	v_and_b32_e32 v144, v149, v144
	v_and_b32_e32 v145, v198, v145
	v_add_f32_e32 v134, v134, v144
	v_add_f32_e32 v149, v134, v145
	v_exp_f32_e32 v134, v200
	s_nop 0
	v_cmp_eq_f32_e32 vcc, 1.0, v134
	v_fma_f32 v245, v245, v134, v149
	s_cmp_eq_u64 vcc, exec
	s_cbranch_scc1 .LBB0_1291
	v_pk_mul_f32 v[30:31], v[30:31], v[134:135] op_sel_hi:[1,0]
	v_pk_mul_f32 v[28:29], v[28:29], v[134:135] op_sel_hi:[1,0]
	v_pk_mul_f32 v[26:27], v[26:27], v[134:135] op_sel_hi:[1,0]
	v_pk_mul_f32 v[24:25], v[24:25], v[134:135] op_sel_hi:[1,0]
	v_pk_mul_f32 v[22:23], v[22:23], v[134:135] op_sel_hi:[1,0]
	v_pk_mul_f32 v[20:21], v[20:21], v[134:135] op_sel_hi:[1,0]
	v_pk_mul_f32 v[18:19], v[18:19], v[134:135] op_sel_hi:[1,0]
	v_pk_mul_f32 v[16:17], v[16:17], v[134:135] op_sel_hi:[1,0]
	v_pk_mul_f32 v[14:15], v[14:15], v[134:135] op_sel_hi:[1,0]
	v_pk_mul_f32 v[12:13], v[12:13], v[134:135] op_sel_hi:[1,0]
	v_pk_mul_f32 v[10:11], v[10:11], v[134:135] op_sel_hi:[1,0]
	v_pk_mul_f32 v[8:9], v[8:9], v[134:135] op_sel_hi:[1,0]
	v_pk_mul_f32 v[6:7], v[6:7], v[134:135] op_sel_hi:[1,0]
	v_pk_mul_f32 v[4:5], v[4:5], v[134:135] op_sel_hi:[1,0]
	v_pk_mul_f32 v[2:3], v[2:3], v[134:135] op_sel_hi:[1,0]
	v_pk_mul_f32 v[0:1], v[0:1], v[134:135] op_sel_hi:[1,0]
.LBB0_1291:
	v_cvt_pk_bf16_f32 v162, v162, v163
	v_cvt_pk_bf16_f32 v163, v164, v165
	v_cvt_pk_bf16_f32 v164, v158, v159
	v_cvt_pk_bf16_f32 v165, v160, v161
	v_cvt_pk_bf16_f32 v158, v218, v167
	v_cvt_pk_bf16_f32 v159, v136, v135
	v_cvt_pk_bf16_f32 v160, v138, v137
	v_cvt_pk_bf16_f32 v161, v140, v139
	v_mfma_f32_16x16x32_bf16 v[54:57], v[106:109], v[162:165], v[54:57]
	v_cvt_pk_bf16_f32 v154, v154, v155
	v_cvt_pk_bf16_f32 v155, v216, v157
	v_cvt_pk_bf16_f32 v156, v156, v151
	v_mfma_f32_16x16x32_bf16 v[16:19], v[106:109], v[158:161], v[16:19]
	v_cvt_pk_bf16_f32 v157, v152, v153
	v_add_u32_e32 v108, v187, v239
	s_add_i32 s18, s18, 1
	v_mfma_f32_16x16x32_bf16 v[66:69], v[130:133], v[162:165], v[66:69]
	v_add_u32_e32 v213, 8, v213
	s_cmp_eq_u32 s17, s18
	v_mfma_f32_16x16x32_bf16 v[28:31], v[130:133], v[158:161], v[28:31]
	v_cvt_pk_bf16_f32 v130, v146, v141
	v_cvt_pk_bf16_f32 v131, v148, v147
	v_cvt_pk_bf16_f32 v132, v142, v143
	v_cvt_pk_bf16_f32 v133, v144, v145
	v_mfma_f32_16x16x32_bf16 v[54:57], v[102:105], v[154:157], v[54:57]
	s_nop 0
	v_mfma_f32_16x16x32_bf16 v[16:19], v[102:105], v[130:133], v[16:19]
	ds_read_b64_tr_b16 v[102:103], v108 offset:32768
	ds_read_b64_tr_b16 v[104:105], v108 offset:36864
	ds_read_b64_tr_b16 v[106:107], v108 offset:40960
	ds_read_b64_tr_b16 v[108:109], v108 offset:45056
	v_mfma_f32_16x16x32_bf16 v[58:61], v[118:121], v[162:165], v[58:61]
	v_mfma_f32_16x16x32_bf16 v[20:23], v[118:121], v[158:161], v[20:23]
	s_waitcnt lgkmcnt(2)
	v_mfma_f32_16x16x32_bf16 v[50:53], v[102:105], v[162:165], v[50:53]
	v_mfma_f32_16x16x32_bf16 v[12:15], v[102:105], v[158:161], v[12:15]
	v_mfma_f32_16x16x32_bf16 v[58:61], v[110:113], v[154:157], v[58:61]
	v_mfma_f32_16x16x32_bf16 v[20:23], v[110:113], v[130:133], v[20:23]
	v_add_u32_e32 v110, v187, v240
	s_waitcnt lgkmcnt(0)
	v_mfma_f32_16x16x32_bf16 v[50:53], v[106:109], v[154:157], v[50:53]
	v_mfma_f32_16x16x32_bf16 v[12:15], v[106:109], v[130:133], v[12:15]
	ds_read_b64_tr_b16 v[102:103], v110 offset:32768
	ds_read_b64_tr_b16 v[104:105], v110 offset:36864
	ds_read_b64_tr_b16 v[106:107], v110 offset:40960
	ds_read_b64_tr_b16 v[108:109], v110 offset:45056
	v_add_u32_e32 v110, v187, v241
	s_waitcnt lgkmcnt(2)
	v_mfma_f32_16x16x32_bf16 v[46:49], v[102:105], v[162:165], v[46:49]
	v_mfma_f32_16x16x32_bf16 v[8:11], v[102:105], v[158:161], v[8:11]
	s_waitcnt lgkmcnt(0)
	v_mfma_f32_16x16x32_bf16 v[46:49], v[106:109], v[154:157], v[46:49]
	v_mfma_f32_16x16x32_bf16 v[8:11], v[106:109], v[130:133], v[8:11]
	ds_read_b64_tr_b16 v[102:103], v110 offset:32768
	ds_read_b64_tr_b16 v[104:105], v110 offset:36864
	ds_read_b64_tr_b16 v[106:107], v110 offset:40960
	ds_read_b64_tr_b16 v[108:109], v110 offset:45056
	s_waitcnt lgkmcnt(2)
	v_mfma_f32_16x16x32_bf16 v[38:41], v[102:105], v[162:165], v[38:41]
	v_mfma_f32_16x16x32_bf16 v[4:7], v[102:105], v[158:161], v[4:7]
	v_add_u32_e32 v103, v187, v242
	ds_read_b64_tr_b16 v[110:111], v103 offset:32768
	ds_read_b64_tr_b16 v[112:113], v103 offset:36864
	s_waitcnt lgkmcnt(2)
	v_mfma_f32_16x16x32_bf16 v[38:41], v[106:109], v[154:157], v[38:41]
	v_mfma_f32_16x16x32_bf16 v[4:7], v[106:109], v[130:133], v[4:7]
	ds_read_b64_tr_b16 v[104:105], v103 offset:40960
	ds_read_b64_tr_b16 v[106:107], v103 offset:45056
	s_waitcnt vmcnt(0)
	v_mfma_f32_16x16x32_bf16 v[62:65], v[126:129], v[162:165], v[62:65]
	s_waitcnt lgkmcnt(0)
	s_barrier
	v_mfma_f32_16x16x32_bf16 v[24:27], v[126:129], v[158:161], v[24:27]
	v_mfma_f32_16x16x32_bf16 v[42:45], v[110:113], v[162:165], v[42:45]
	v_mfma_f32_16x16x32_bf16 v[0:3], v[110:113], v[158:161], v[0:3]
	v_mfma_f32_16x16x32_bf16 v[66:69], v[122:125], v[154:157], v[66:69]
	v_mfma_f32_16x16x32_bf16 v[28:31], v[122:125], v[130:133], v[28:31]
	v_mfma_f32_16x16x32_bf16 v[62:65], v[114:117], v[154:157], v[62:65]
	v_mfma_f32_16x16x32_bf16 v[24:27], v[114:117], v[130:133], v[24:27]
	v_mfma_f32_16x16x32_bf16 v[42:45], v[104:107], v[154:157], v[42:45]
	v_mfma_f32_16x16x32_bf16 v[0:3], v[104:107], v[130:133], v[0:3]
	s_cbranch_scc0 .LBB0_1283
	v_mov_b32_e32 v167, v215
	v_mov_b32_e32 v198, v245
	s_nop 1
	v_permlane16_swap_b32_e32 v215, v167
	v_permlane16_swap_b32_e32 v245, v198
	v_add_f32_e32 v167, v215, v167
	v_add_f32_e32 v198, v245, v198
	v_mov_b32_e32 v217, v167
	v_mov_b32_e32 v248, v198
	s_nop 1
	v_permlane32_swap_b32_e32 v167, v217
	v_permlane32_swap_b32_e32 v198, v248
	v_add_f32_e32 v103, v167, v217
	v_add_f32_e32 v102, v198, v248
	s_branch .LBB0_1280

.LBB0_1903:
	s_andn2_b64 vcc, exec, s[0:1]
	s_cbranch_vccnz .LBB0_1968
	s_waitcnt vmcnt(0)
	v_mbcnt_lo_u32_b32 v0, -1, 0
	v_mbcnt_hi_u32_b32 v0, -1, v0
	v_readlane_b32 s0, v253, 8
	v_add_u32_e32 v0, s95, v0
	v_readlane_b32 s8, v251, 0
	v_add_u32_e32 v32, s0, v0
	v_readlane_b32 s0, v251, 10
	v_readlane_b32 s1, v251, 11
	v_readlane_b32 s2, v251, 12
	v_readlane_b32 s3, v251, 13
	s_mov_b64 s[0:1], s[2:3]
	s_add_u32 s2, s0, 0x69b00000
	s_addc_u32 s3, s1, 0
	s_add_u32 s4, s0, 0x71b00000
	v_readlane_b32 s16, v254, 8
	v_readlane_b32 s10, v251, 2
	v_readlane_b32 s11, v251, 3
	s_addc_u32 s5, s1, 0
	v_readlane_b32 s17, v254, 9
	s_mul_i32 s1, s16, 0x18000
	s_mov_b64 s[6:7], s[10:11]
	s_mov_b32 s17, s87
	s_mul_hi_u32 s0, s16, 0x18000
	v_readlane_b32 s9, v251, 1
	v_readlane_b32 s12, v251, 4
	v_readlane_b32 s13, v251, 5
	s_add_u32 s6, s6, s1
	s_mov_b64 s[8:9], s[12:13]
	s_addc_u32 s7, s7, s0
	s_lshl_b64 s[0:1], s[16:17], 15
	s_add_u32 s8, s8, s0
	s_mov_b32 s0, s16
	s_addc_u32 s9, s9, s1
	v_writelane_b32 v254, s0, 8
	s_cmp_gt_u32 s16, 1
	v_readlane_b32 s14, v251, 6
	v_writelane_b32 v254, s1, 9
	s_mov_b32 s0, 0x80000
	v_cmp_gt_i32_e64 s[34:35], s0, v32
	s_mov_b64 s[0:1], -1
	v_readlane_b32 s15, v251, 7
	s_cbranch_scc1 .LBB0_1909
	s_and_saveexec_b64 s[10:11], s[34:35]
	s_cbranch_execz .LBB0_1908
	s_add_u32 s12, s8, 0x4000
	s_addc_u32 s13, s9, 0
	s_add_u32 s14, s6, 0x4000
	s_addc_u32 s15, s7, 0
	s_add_u32 s16, s6, 0x8000
	s_addc_u32 s17, s7, 0
	s_add_u32 s18, s6, 0xc000
	s_addc_u32 s19, s7, 0
	s_add_u32 s20, s6, 0x10000
	s_addc_u32 s21, s7, 0
	s_add_u32 s22, s6, 0x14000
	s_addc_u32 s23, s7, 0
	v_lshlrev_b32_e32 v194, 3, v32
	s_lshl_b32 s26, s71, 3
	s_mov_b64 s[24:25], 0
	v_mov_b32_e32 v195, v32
	s_add_u32 s100, s2, 0x2000
	s_addc_u32 s101, s3, 0
.LBB0_1907:
	v_ashrrev_i32_e32 v0, 31, v195
	v_lshrrev_b32_e32 v0, 23, v0
	v_add_u32_e32 v0, v195, v0
	v_ashrrev_i32_e32 v0, 9, v0
	v_mul_i32_i24_e32 v1, 0x200, v0
	v_lshlrev_b32_e32 v1, 3, v1
	v_sub_u32_e32 v70, v194, v1
	v_lshlrev_b32_e32 v150, 3, v0
	v_ashrrev_i32_e32 v71, 31, v70
	v_and_b32_e32 v224, 0xff8, v150
	v_lshlrev_b64 v[46:47], 2, v[70:71]
	v_cmp_eq_u32_e32 vcc, 0, v224
	v_lshl_add_u64 v[0:1], s[6:7], 0, v[46:47]
	global_load_dwordx4 v[54:57], v[0:1], off offset:16
	global_load_dwordx4 v[58:61], v[0:1], off
	v_lshl_add_u64 v[0:1], s[14:15], 0, v[46:47]
	global_load_dwordx4 v[24:27], v[0:1], off offset:16
	global_load_dwordx4 v[42:45], v[0:1], off
	v_lshl_add_u64 v[0:1], s[16:17], 0, v[46:47]
	v_lshlrev_b64 v[134:135], 1, v[70:71]
	global_load_dwordx4 v[20:23], v[0:1], off offset:16
	global_load_dwordx4 v[38:41], v[0:1], off
	v_lshl_add_u64 v[0:1], s[18:19], 0, v[46:47]
	global_load_dwordx4 v[16:19], v[0:1], off offset:16
	global_load_dwordx4 v[28:31], v[0:1], off
	v_lshl_add_u64 v[0:1], s[20:21], 0, v[46:47]
	v_lshl_add_u64 v[8:9], s[22:23], 0, v[46:47]
	v_lshl_add_u64 v[48:49], s[8:9], 0, v[46:47]
	v_lshl_add_u64 v[50:51], s[12:13], 0, v[46:47]
	s_waitcnt lgkmcnt(0)
	global_load_dwordx4 v[4:7], v[0:1], off offset:16
	global_load_dwordx4 v[12:15], v[0:1], off
	s_nop 0
	global_load_dwordx4 v[0:3], v[8:9], off offset:16
	s_nop 0
	global_load_dwordx4 v[8:11], v[8:9], off
	s_nop 0
	global_load_dwordx4 v[62:65], v[48:49], off offset:16
	global_load_dwordx4 v[66:69], v[48:49], off
	s_nop 0
	global_load_dwordx4 v[46:49], v[50:51], off offset:16
	s_nop 0
	global_load_dwordx4 v[50:53], v[50:51], off
	v_ashrrev_i32_e32 v151, 31, v150
	v_cndmask_b32_e64 v213, 2, 0, vcc
	v_lshl_add_u32 v212, v150, 14, v134
	v_lshlrev_b32_e32 v214, 13, v213
	v_lshlrev_b32_e32 v213, 14, v213
	v_sub_u32_e32 v213, v212, v213
	v_sub_u32_e32 v214, v212, v214
	global_load_dwordx4 v[216:219], v213, s[2:3]
	global_load_dwordx4 v[220:223], v213, s[100:101]
	global_load_dwordx4 v[200:203], v214, s[2:3]
	global_load_dwordx4 v[208:211], v214, s[100:101]
	global_load_dwordx4 v[130:133], v212, s[2:3]
	global_load_dwordx4 v[126:129], v212, s[100:101]
	v_add_u32_e32 v213, 0x4000, v212
	global_load_dwordx4 v[122:125], v213, s[2:3]
	global_load_dwordx4 v[118:121], v213, s[100:101]
	v_add_u32_e32 v214, 0x8000, v212
	global_load_dwordx4 v[114:117], v214, s[2:3]
	global_load_dwordx4 v[110:113], v214, s[100:101]
	v_add_u32_e32 v213, 0xc000, v212
	global_load_dwordx4 v[106:109], v213, s[2:3]
	global_load_dwordx4 v[102:105], v213, s[100:101]
	v_add_u32_e32 v214, 0x10000, v212
	global_load_dwordx4 v[98:101], v214, s[2:3]
	global_load_dwordx4 v[94:97], v214, s[100:101]
	v_add_u32_e32 v213, 0x14000, v212
	global_load_dwordx4 v[90:93], v213, s[2:3]
	global_load_dwordx4 v[86:89], v213, s[100:101]
	v_add_u32_e32 v214, 0x18000, v212
	global_load_dwordx4 v[82:85], v214, s[2:3]
	global_load_dwordx4 v[78:81], v214, s[100:101]
	v_add_u32_e32 v213, 0x1c000, v212
	global_load_dwordx4 v[70:73], v213, s[100:101]
	global_load_dwordx4 v[74:77], v213, s[2:3]
	v_or_b32_e32 v148, 1, v150
	s_nop 0
	v_ashrrev_i32_e32 v149, 31, v148
	v_or_b32_e32 v146, 2, v150
	v_ashrrev_i32_e32 v147, 31, v146
	v_or_b32_e32 v144, 3, v150
	v_ashrrev_i32_e32 v145, 31, v144
	v_or_b32_e32 v142, 4, v150
	v_ashrrev_i32_e32 v143, 31, v142
	v_or_b32_e32 v140, 5, v150
	v_ashrrev_i32_e32 v141, 31, v140
	v_or_b32_e32 v138, 6, v150
	v_ashrrev_i32_e32 v139, 31, v138
	v_or_b32_e32 v136, 7, v150
	v_ashrrev_i32_e32 v137, 31, v136
	v_lshl_add_u64 v[134:135], s[4:5], 0, v[134:135]
	v_add_u32_e32 v195, s71, v195
	v_add_u32_e32 v194, s26, v194
	s_waitcnt vmcnt(19)
	v_cndmask_b32_e64 v161, v219, 0, vcc
	v_cndmask_b32_e64 v164, v218, 0, vcc
	v_cndmask_b32_e64 v166, v217, 0, vcc
	v_cndmask_b32_e64 v167, v216, 0, vcc
	v_lshlrev_b32_e32 v168, 16, v167
	v_and_b32_e32 v169, 0xffff0000, v167
	s_waitcnt vmcnt(18)
	v_cndmask_b32_e64 v156, v223, 0, vcc
	v_cndmask_b32_e64 v159, v222, 0, vcc
	v_cndmask_b32_e64 v162, v221, 0, vcc
	v_cndmask_b32_e64 v165, v220, 0, vcc
	v_cmp_ne_u32_e32 vcc, 0, v224
	v_lshlrev_b32_e32 v170, 16, v166
	v_and_b32_e32 v171, 0xffff0000, v166
	v_lshlrev_b32_e32 v166, 16, v164
	s_nop 0
	v_and_b32_e32 v167, 0xffff0000, v164
	v_lshlrev_b32_e32 v172, 16, v161
	v_and_b32_e32 v173, 0xffff0000, v161
	v_lshlrev_b32_e32 v164, 16, v165
	v_and_b32_e32 v165, 0xffff0000, v165
	v_lshlrev_b32_e32 v174, 16, v162
	v_and_b32_e32 v175, 0xffff0000, v162
	v_lshlrev_b32_e32 v176, 16, v159
	v_and_b32_e32 v177, 0xffff0000, v159
	v_lshlrev_b32_e32 v178, 16, v156
	v_and_b32_e32 v179, 0xffff0000, v156
	v_pk_fma_f32 v[182:183], v[58:59], v[168:169], v[66:67]
	v_pk_fma_f32 v[180:181], v[60:61], v[170:171], v[68:69]
	v_pk_fma_f32 v[184:185], v[56:57], v[172:173], v[64:65]
	v_pk_fma_f32 v[188:189], v[54:55], v[166:167], v[62:63]
	v_pk_fma_f32 v[190:191], v[44:45], v[174:175], v[52:53]
	v_pk_fma_f32 v[192:193], v[42:43], v[164:165], v[50:51]
	v_pk_fma_f32 v[196:197], v[26:27], v[178:179], v[48:49]
	v_pk_fma_f32 v[198:199], v[24:25], v[176:177], v[46:47]
	s_waitcnt vmcnt(17)
	v_cndmask_b32_e32 v160, 0, v201, vcc
	v_cndmask_b32_e32 v163, 0, v200, vcc
	v_cndmask_b32_e32 v154, 0, v203, vcc
	v_cndmask_b32_e32 v157, 0, v202, vcc
	s_waitcnt vmcnt(16)
	v_cndmask_b32_e32 v152, 0, v211, vcc
	v_cndmask_b32_e32 v153, 0, v210, vcc
	v_cndmask_b32_e32 v155, 0, v209, vcc
	v_cndmask_b32_e32 v158, 0, v208, vcc
	v_lshlrev_b32_e32 v162, 16, v163
	s_nop 0
	v_and_b32_e32 v163, 0xffff0000, v163
	s_nop 0
	v_lshlrev_b32_e32 v166, 16, v160
	v_and_b32_e32 v167, 0xffff0000, v160
	v_lshlrev_b32_e32 v164, 16, v157
	v_and_b32_e32 v165, 0xffff0000, v157
	v_lshlrev_b32_e32 v170, 16, v154
	v_and_b32_e32 v171, 0xffff0000, v154
	v_lshlrev_b32_e32 v168, 16, v158
	v_and_b32_e32 v169, 0xffff0000, v158
	v_lshlrev_b32_e32 v174, 16, v155
	v_and_b32_e32 v175, 0xffff0000, v155
	v_lshlrev_b32_e32 v172, 16, v153
	v_and_b32_e32 v173, 0xffff0000, v153
	v_lshlrev_b32_e32 v176, 16, v152
	v_and_b32_e32 v177, 0xffff0000, v152
	v_pk_fma_f32 v[178:179], v[38:39], v[162:163], v[182:183]
	v_pk_fma_f32 v[186:187], v[40:41], v[166:167], v[180:181]
	v_pk_fma_f32 v[180:181], v[20:21], v[164:165], v[188:189]
	v_pk_fma_f32 v[188:189], v[22:23], v[170:171], v[184:185]
	v_pk_fma_f32 v[182:183], v[28:29], v[168:169], v[192:193]
	v_pk_fma_f32 v[190:191], v[30:31], v[174:175], v[190:191]
	v_pk_fma_f32 v[192:193], v[18:19], v[176:177], v[196:197]
	v_pk_fma_f32 v[184:185], v[16:17], v[172:173], v[198:199]
	s_nop 0
	v_pk_fma_f32 v[164:165], v[54:55], v[164:165], v[62:63]
	s_nop 0
	s_waitcnt vmcnt(15)
	v_lshlrev_b32_e32 v152, 16, v130
	v_and_b32_e32 v153, 0xffff0000, v130
	v_lshlrev_b32_e32 v154, 16, v131
	v_and_b32_e32 v155, 0xffff0000, v131
	v_lshlrev_b32_e32 v156, 16, v133
	v_and_b32_e32 v157, 0xffff0000, v133
	v_pk_fma_f32 v[178:179], v[12:13], v[152:153], v[178:179]
	v_lshlrev_b32_e32 v130, 16, v132
	v_and_b32_e32 v131, 0xffff0000, v132
	v_pk_fma_f32 v[180:181], v[4:5], v[130:131], v[180:181]
	s_waitcnt vmcnt(14)
	v_lshlrev_b32_e32 v158, 16, v127
	v_and_b32_e32 v159, 0xffff0000, v127
	v_lshlrev_b32_e32 v160, 16, v129
	v_and_b32_e32 v161, 0xffff0000, v129
	v_lshlrev_b32_e32 v132, 16, v126
	v_and_b32_e32 v133, 0xffff0000, v126
	v_lshlrev_b32_e32 v126, 16, v128
	v_and_b32_e32 v127, 0xffff0000, v128
	v_pk_fma_f32 v[128:129], v[14:15], v[154:155], v[186:187]
	v_pk_fma_f32 v[186:187], v[6:7], v[156:157], v[188:189]
	v_pk_fma_f32 v[188:189], v[10:11], v[158:159], v[190:191]
	v_pk_fma_f32 v[190:191], v[2:3], v[160:161], v[192:193]
	v_mul_f32_e32 v192, 0x3d372713, v178
	v_mul_f32_e32 v193, 0x3d372713, v179
	v_mul_f32_e32 v192, v178, v192
	v_mul_f32_e32 v193, v179, v193
	v_fma_f32 v192, v178, v192, v178
	v_fma_f32 v193, v179, v193, v179
	v_mul_f32_e32 v192, 0x3f4c422a, v192
	v_mul_f32_e32 v193, 0x3f4c422a, v193
	v_mul_f32_e32 v192, -2.0, v192
	v_mul_f32_e32 v193, -2.0, v193
	v_mul_f32_e32 v192, 0x3fb8aa3b, v192
	v_mul_f32_e32 v193, 0x3fb8aa3b, v193
	v_exp_f32_e32 v192, v192
	v_exp_f32_e32 v193, v193
	v_pk_fma_f32 v[182:183], v[8:9], v[132:133], v[182:183]
	v_add_f32_e32 v192, 1.0, v192
	v_add_f32_e32 v193, 1.0, v193
	v_rcp_f32_e32 v192, v192
	v_rcp_f32_e32 v193, v193
	s_nop 0
	v_pk_mul_f32 v[178:179], v[178:179], v[192:193]
	v_pk_mul_f32 v[178:179], v[182:183], v[178:179]
	v_mul_f32_e32 v182, 0x3d372713, v128
	v_mul_f32_e32 v183, 0x3d372713, v129
	v_mul_f32_e32 v182, v128, v182
	v_mul_f32_e32 v183, v129, v183
	v_fma_f32 v182, v128, v182, v128
	v_fma_f32 v183, v129, v183, v129
	v_mul_f32_e32 v182, 0x3f4c422a, v182
	v_mul_f32_e32 v183, 0x3f4c422a, v183
	v_mul_f32_e32 v182, -2.0, v182
	v_mul_f32_e32 v183, -2.0, v183
	v_mul_f32_e32 v182, 0x3fb8aa3b, v182
	v_mul_f32_e32 v183, 0x3fb8aa3b, v183
	v_exp_f32_e32 v182, v182
	v_exp_f32_e32 v183, v183
	v_add_f32_e32 v182, 1.0, v182
	v_add_f32_e32 v183, 1.0, v183
	v_rcp_f32_e32 v182, v182
	v_rcp_f32_e32 v183, v183
	s_nop 0
	v_pk_mul_f32 v[128:129], v[128:129], v[182:183]
	v_mul_f32_e32 v182, 0x3d372713, v180
	v_mul_f32_e32 v183, 0x3d372713, v181
	v_mul_f32_e32 v182, v180, v182
	v_mul_f32_e32 v183, v181, v183
	v_fma_f32 v182, v180, v182, v180
	v_fma_f32 v183, v181, v183, v181
	v_mul_f32_e32 v182, 0x3f4c422a, v182
	v_mul_f32_e32 v183, 0x3f4c422a, v183
	v_mul_f32_e32 v182, -2.0, v182
	v_mul_f32_e32 v183, -2.0, v183
	v_mul_f32_e32 v182, 0x3fb8aa3b, v182
	v_mul_f32_e32 v183, 0x3fb8aa3b, v183
	v_exp_f32_e32 v182, v182
	v_exp_f32_e32 v183, v183
	v_add_f32_e32 v182, 1.0, v182
	v_add_f32_e32 v183, 1.0, v183
	v_rcp_f32_e32 v182, v182
	v_rcp_f32_e32 v183, v183
	s_nop 0
	v_pk_mul_f32 v[180:181], v[180:181], v[182:183]
	v_mul_f32_e32 v182, 0x3d372713, v186
	v_mul_f32_e32 v183, 0x3d372713, v187
	v_mul_f32_e32 v182, v186, v182
	v_mul_f32_e32 v183, v187, v183
	v_fma_f32 v182, v186, v182, v186
	v_fma_f32 v183, v187, v183, v187
	v_mul_f32_e32 v182, 0x3f4c422a, v182
	v_mul_f32_e32 v183, 0x3f4c422a, v183
	v_mul_f32_e32 v182, -2.0, v182
	v_mul_f32_e32 v183, -2.0, v183
	v_mul_f32_e32 v182, 0x3fb8aa3b, v182
	v_mul_f32_e32 v183, 0x3fb8aa3b, v183
	v_exp_f32_e32 v182, v182
	v_exp_f32_e32 v183, v183
	v_add_f32_e32 v182, 1.0, v182
	v_add_f32_e32 v183, 1.0, v183
	v_rcp_f32_e32 v182, v182
	v_rcp_f32_e32 v183, v183
	v_pk_fma_f32 v[184:185], v[0:1], v[126:127], v[184:185]
	v_pk_mul_f32 v[128:129], v[188:189], v[128:129]
	v_pk_mul_f32 v[182:183], v[186:187], v[182:183]
	v_pk_mul_f32 v[180:181], v[184:185], v[180:181]
	v_pk_mul_f32 v[182:183], v[190:191], v[182:183]
	v_cvt_pk_bf16_f32 v178, v178, v179
	v_cvt_pk_bf16_f32 v179, v128, v129
	v_lshlrev_b64 v[128:129], 13, v[150:151]
	v_cvt_pk_bf16_f32 v180, v180, v181
	v_cvt_pk_bf16_f32 v181, v182, v183
	v_lshl_add_u64 v[128:129], v[134:135], 0, v[128:129]
	s_nop 0
	v_pk_fma_f32 v[150:151], v[58:59], v[162:163], v[66:67]
	global_store_dwordx4 v[128:129], v[178:181], off
	v_pk_fma_f32 v[128:129], v[60:61], v[166:167], v[68:69]
	v_pk_fma_f32 v[162:163], v[56:57], v[170:171], v[64:65]
	v_pk_fma_f32 v[166:167], v[44:45], v[174:175], v[52:53]
	v_pk_fma_f32 v[174:175], v[42:43], v[168:169], v[50:51]
	v_pk_fma_f32 v[182:183], v[26:27], v[176:177], v[48:49]
	v_pk_fma_f32 v[168:169], v[38:39], v[152:153], v[150:151]
	v_pk_fma_f32 v[176:177], v[40:41], v[154:155], v[128:129]
	s_waitcnt vmcnt(14)
	v_lshlrev_b32_e32 v128, 16, v122
	v_and_b32_e32 v129, 0xffff0000, v122
	v_pk_fma_f32 v[170:171], v[20:21], v[130:131], v[164:165]
	v_pk_fma_f32 v[178:179], v[22:23], v[156:157], v[162:163]
	v_pk_fma_f32 v[180:181], v[30:31], v[158:159], v[166:167]
	v_pk_fma_f32 v[182:183], v[18:19], v[160:161], v[182:183]
	v_lshlrev_b32_e32 v150, 16, v123
	v_and_b32_e32 v151, 0xffff0000, v123
	v_lshlrev_b32_e32 v162, 16, v125
	v_and_b32_e32 v163, 0xffff0000, v125
	s_waitcnt vmcnt(13)
	v_lshlrev_b32_e32 v164, 16, v119
	v_and_b32_e32 v165, 0xffff0000, v119
	v_lshlrev_b32_e32 v166, 16, v121
	v_and_b32_e32 v167, 0xffff0000, v121
	v_pk_fma_f32 v[168:169], v[12:13], v[128:129], v[168:169]
	v_lshlrev_b32_e32 v122, 16, v124
	v_and_b32_e32 v123, 0xffff0000, v124
	v_lshlrev_b32_e32 v124, 16, v118
	v_and_b32_e32 v125, 0xffff0000, v118
	v_lshlrev_b32_e32 v118, 16, v120
	v_and_b32_e32 v119, 0xffff0000, v120
	v_pk_fma_f32 v[120:121], v[14:15], v[150:151], v[176:177]
	v_pk_fma_f32 v[176:177], v[6:7], v[162:163], v[178:179]
	v_pk_fma_f32 v[178:179], v[10:11], v[164:165], v[180:181]
	v_pk_fma_f32 v[180:181], v[2:3], v[166:167], v[182:183]
	v_mul_f32_e32 v182, 0x3d372713, v168
	v_mul_f32_e32 v183, 0x3d372713, v169
	v_mul_f32_e32 v182, v168, v182
	v_mul_f32_e32 v183, v169, v183
	v_fma_f32 v182, v168, v182, v168
	v_fma_f32 v183, v169, v183, v169
	v_mul_f32_e32 v182, 0x3f4c422a, v182
	v_mul_f32_e32 v183, 0x3f4c422a, v183
	v_mul_f32_e32 v182, -2.0, v182
	v_mul_f32_e32 v183, -2.0, v183
	v_mul_f32_e32 v182, 0x3fb8aa3b, v182
	v_mul_f32_e32 v183, 0x3fb8aa3b, v183
	v_exp_f32_e32 v182, v182
	v_exp_f32_e32 v183, v183
	v_pk_fma_f32 v[184:185], v[24:25], v[172:173], v[46:47]
	v_pk_fma_f32 v[172:173], v[28:29], v[132:133], v[174:175]
	v_add_f32_e32 v182, 1.0, v182
	v_add_f32_e32 v183, 1.0, v183
	v_rcp_f32_e32 v182, v182
	v_rcp_f32_e32 v183, v183
	v_pk_fma_f32 v[172:173], v[8:9], v[124:125], v[172:173]
	v_pk_fma_f32 v[170:171], v[4:5], v[122:123], v[170:171]
	v_pk_fma_f32 v[174:175], v[16:17], v[126:127], v[184:185]
	v_pk_mul_f32 v[168:169], v[168:169], v[182:183]
	v_pk_fma_f32 v[174:175], v[0:1], v[118:119], v[174:175]
	v_pk_mul_f32 v[168:169], v[172:173], v[168:169]
	v_mul_f32_e32 v172, 0x3d372713, v120
	v_mul_f32_e32 v173, 0x3d372713, v121
	v_mul_f32_e32 v172, v120, v172
	v_mul_f32_e32 v173, v121, v173
	v_fma_f32 v172, v120, v172, v120
	v_fma_f32 v173, v121, v173, v121
	v_mul_f32_e32 v172, 0x3f4c422a, v172
	v_mul_f32_e32 v173, 0x3f4c422a, v173
	v_mul_f32_e32 v172, -2.0, v172
	v_mul_f32_e32 v173, -2.0, v173
	v_mul_f32_e32 v172, 0x3fb8aa3b, v172
	v_mul_f32_e32 v173, 0x3fb8aa3b, v173
	v_exp_f32_e32 v172, v172
	v_exp_f32_e32 v173, v173
	v_cvt_pk_bf16_f32 v168, v168, v169
	v_pk_fma_f32 v[132:133], v[42:43], v[132:133], v[50:51]
	v_add_f32_e32 v172, 1.0, v172
	v_add_f32_e32 v173, 1.0, v173
	v_rcp_f32_e32 v172, v172
	v_rcp_f32_e32 v173, v173
	v_pk_fma_f32 v[126:127], v[24:25], v[126:127], v[46:47]
	v_cmp_lt_i32_e32 vcc, s79, v195
	s_or_b64 s[24:25], vcc, s[24:25]
	v_pk_mul_f32 v[120:121], v[120:121], v[172:173]
	v_mul_f32_e32 v172, 0x3d372713, v170
	v_mul_f32_e32 v173, 0x3d372713, v171
	v_mul_f32_e32 v172, v170, v172
	v_mul_f32_e32 v173, v171, v173
	v_fma_f32 v172, v170, v172, v170
	v_fma_f32 v173, v171, v173, v171
	v_mul_f32_e32 v172, 0x3f4c422a, v172
	v_mul_f32_e32 v173, 0x3f4c422a, v173
	v_mul_f32_e32 v172, -2.0, v172
	v_mul_f32_e32 v173, -2.0, v173
	v_mul_f32_e32 v172, 0x3fb8aa3b, v172
	v_mul_f32_e32 v173, 0x3fb8aa3b, v173
	v_exp_f32_e32 v172, v172
	v_exp_f32_e32 v173, v173
	v_pk_mul_f32 v[120:121], v[178:179], v[120:121]
	v_add_f32_e32 v172, 1.0, v172
	v_add_f32_e32 v173, 1.0, v173
	v_rcp_f32_e32 v172, v172
	v_rcp_f32_e32 v173, v173
	v_cvt_pk_bf16_f32 v169, v120, v121
	v_lshlrev_b64 v[120:121], 13, v[148:149]
	v_lshl_add_u64 v[120:121], v[134:135], 0, v[120:121]
	v_pk_mul_f32 v[170:171], v[170:171], v[172:173]
	v_mul_f32_e32 v172, 0x3d372713, v176
	v_mul_f32_e32 v173, 0x3d372713, v177
	v_mul_f32_e32 v172, v176, v172
	v_mul_f32_e32 v173, v177, v173
	v_fma_f32 v172, v176, v172, v176
	v_fma_f32 v173, v177, v173, v177
	v_mul_f32_e32 v172, 0x3f4c422a, v172
	v_mul_f32_e32 v173, 0x3f4c422a, v173
	v_mul_f32_e32 v172, -2.0, v172
	v_mul_f32_e32 v173, -2.0, v173
	v_mul_f32_e32 v172, 0x3fb8aa3b, v172
	v_mul_f32_e32 v173, 0x3fb8aa3b, v173
	v_exp_f32_e32 v172, v172
	v_exp_f32_e32 v173, v173
	v_pk_mul_f32 v[170:171], v[174:175], v[170:171]
	v_pk_fma_f32 v[148:149], v[58:59], v[152:153], v[66:67]
	v_add_f32_e32 v172, 1.0, v172
	v_add_f32_e32 v173, 1.0, v173
	v_rcp_f32_e32 v172, v172
	v_rcp_f32_e32 v173, v173
	v_cvt_pk_bf16_f32 v170, v170, v171
	v_pk_fma_f32 v[152:153], v[56:57], v[156:157], v[64:65]
	v_pk_fma_f32 v[156:157], v[44:45], v[158:159], v[52:53]
	v_pk_mul_f32 v[172:173], v[176:177], v[172:173]
	s_nop 0
	v_pk_mul_f32 v[172:173], v[180:181], v[172:173]
	s_nop 0
	v_cvt_pk_bf16_f32 v171, v172, v173
	global_store_dwordx4 v[120:121], v[168:171], off
	v_pk_fma_f32 v[120:121], v[60:61], v[154:155], v[68:69]
	v_pk_fma_f32 v[154:155], v[54:55], v[130:131], v[62:63]
	v_pk_fma_f32 v[130:131], v[38:39], v[128:129], v[148:149]
	v_pk_fma_f32 v[158:159], v[40:41], v[150:151], v[120:121]
	s_waitcnt vmcnt(13)
	v_lshlrev_b32_e32 v120, 16, v114
	v_and_b32_e32 v121, 0xffff0000, v114
	v_pk_fma_f32 v[130:131], v[12:13], v[120:121], v[130:131]
	v_pk_fma_f32 v[148:149], v[20:21], v[122:123], v[154:155]
	v_mul_f32_e32 v172, 0x3d372713, v130
	v_mul_f32_e32 v173, 0x3d372713, v131
	v_mul_f32_e32 v172, v130, v172
	v_mul_f32_e32 v173, v131, v173
	v_fma_f32 v172, v130, v172, v130
	v_fma_f32 v173, v131, v173, v131
	v_mul_f32_e32 v172, 0x3f4c422a, v172
	v_mul_f32_e32 v173, 0x3f4c422a, v173
	v_mul_f32_e32 v172, -2.0, v172
	v_mul_f32_e32 v173, -2.0, v173
	v_mul_f32_e32 v172, 0x3fb8aa3b, v172
	v_mul_f32_e32 v173, 0x3fb8aa3b, v173
	v_exp_f32_e32 v172, v172
	v_exp_f32_e32 v173, v173
	v_pk_fma_f32 v[154:155], v[28:29], v[124:125], v[132:133]
	v_pk_fma_f32 v[168:169], v[30:31], v[164:165], v[156:157]
	v_add_f32_e32 v172, 1.0, v172
	v_add_f32_e32 v173, 1.0, v173
	v_rcp_f32_e32 v172, v172
	v_rcp_f32_e32 v173, v173
	v_pk_fma_f32 v[156:157], v[16:17], v[118:119], v[126:127]
	v_lshlrev_b32_e32 v126, 16, v115
	v_and_b32_e32 v127, 0xffff0000, v115
	v_lshlrev_b32_e32 v114, 16, v116
	v_and_b32_e32 v115, 0xffff0000, v116
	v_lshlrev_b32_e32 v132, 16, v117
	v_and_b32_e32 v133, 0xffff0000, v117
	s_waitcnt vmcnt(12)
	v_lshlrev_b32_e32 v116, 16, v110
	v_and_b32_e32 v117, 0xffff0000, v110
	v_pk_fma_f32 v[158:159], v[14:15], v[126:127], v[158:159]
	v_pk_fma_f32 v[154:155], v[8:9], v[116:117], v[154:155]
	v_pk_mul_f32 v[130:131], v[130:131], v[172:173]
	v_pk_fma_f32 v[170:171], v[26:27], v[160:161], v[48:49]
	v_pk_mul_f32 v[130:131], v[154:155], v[130:131]
	v_mul_f32_e32 v154, 0x3d372713, v158
	v_mul_f32_e32 v155, 0x3d372713, v159
	v_mul_f32_e32 v154, v158, v154
	v_mul_f32_e32 v155, v159, v155
	v_fma_f32 v154, v158, v154, v158
	v_fma_f32 v155, v159, v155, v159
	v_mul_f32_e32 v154, 0x3f4c422a, v154
	v_mul_f32_e32 v155, 0x3f4c422a, v155
	v_mul_f32_e32 v154, -2.0, v154
	v_mul_f32_e32 v155, -2.0, v155
	v_mul_f32_e32 v154, 0x3fb8aa3b, v154
	v_mul_f32_e32 v155, 0x3fb8aa3b, v155
	v_exp_f32_e32 v154, v154
	v_exp_f32_e32 v155, v155
	v_pk_fma_f32 v[160:161], v[22:23], v[162:163], v[152:153]
	v_lshlrev_b32_e32 v152, 16, v111
	v_add_f32_e32 v154, 1.0, v154
	v_add_f32_e32 v155, 1.0, v155
	v_rcp_f32_e32 v154, v154
	v_rcp_f32_e32 v155, v155
	v_and_b32_e32 v153, 0xffff0000, v111
	v_pk_fma_f32 v[148:149], v[4:5], v[114:115], v[148:149]
	v_pk_fma_f32 v[168:169], v[10:11], v[152:153], v[168:169]
	v_pk_mul_f32 v[154:155], v[158:159], v[154:155]
	v_pk_fma_f32 v[160:161], v[6:7], v[132:133], v[160:161]
	v_pk_mul_f32 v[158:159], v[168:169], v[154:155]
	v_mul_f32_e32 v154, 0x3d372713, v148
	v_mul_f32_e32 v155, 0x3d372713, v149
	v_mul_f32_e32 v154, v148, v154
	v_mul_f32_e32 v155, v149, v155
	v_fma_f32 v154, v148, v154, v148
	v_fma_f32 v155, v149, v155, v149
	v_mul_f32_e32 v154, 0x3f4c422a, v154
	v_mul_f32_e32 v155, 0x3f4c422a, v155
	v_mul_f32_e32 v154, -2.0, v154
	v_mul_f32_e32 v155, -2.0, v155
	v_mul_f32_e32 v154, 0x3fb8aa3b, v154
	v_mul_f32_e32 v155, 0x3fb8aa3b, v155
	v_exp_f32_e32 v154, v154
	v_exp_f32_e32 v155, v155
	v_pk_fma_f32 v[170:171], v[18:19], v[166:167], v[170:171]
	v_lshlrev_b32_e32 v110, 16, v112
	v_add_f32_e32 v154, 1.0, v154
	v_add_f32_e32 v155, 1.0, v155
	v_rcp_f32_e32 v154, v154
	v_rcp_f32_e32 v155, v155
	v_and_b32_e32 v111, 0xffff0000, v112
	v_lshlrev_b32_e32 v112, 16, v113
	v_and_b32_e32 v113, 0xffff0000, v113
	v_pk_mul_f32 v[148:149], v[148:149], v[154:155]
	v_mul_f32_e32 v154, 0x3d372713, v160
	v_mul_f32_e32 v155, 0x3d372713, v161
	v_mul_f32_e32 v154, v160, v154
	v_mul_f32_e32 v155, v161, v155
	v_fma_f32 v154, v160, v154, v160
	v_fma_f32 v155, v161, v155, v161
	v_mul_f32_e32 v154, 0x3f4c422a, v154
	v_mul_f32_e32 v155, 0x3f4c422a, v155
	v_mul_f32_e32 v154, -2.0, v154
	v_mul_f32_e32 v155, -2.0, v155
	v_mul_f32_e32 v154, 0x3fb8aa3b, v154
	v_mul_f32_e32 v155, 0x3fb8aa3b, v155
	v_exp_f32_e32 v154, v154
	v_exp_f32_e32 v155, v155
	v_pk_fma_f32 v[170:171], v[2:3], v[112:113], v[170:171]
	v_pk_fma_f32 v[156:157], v[0:1], v[110:111], v[156:157]
	v_add_f32_e32 v154, 1.0, v154
	v_add_f32_e32 v155, 1.0, v155
	v_rcp_f32_e32 v154, v154
	v_rcp_f32_e32 v155, v155
	v_pk_mul_f32 v[148:149], v[156:157], v[148:149]
	v_pk_fma_f32 v[128:129], v[58:59], v[128:129], v[66:67]
	v_cvt_pk_bf16_f32 v156, v148, v149
	v_pk_mul_f32 v[154:155], v[160:161], v[154:155]
	v_pk_fma_f32 v[118:119], v[24:25], v[118:119], v[46:47]
	v_pk_mul_f32 v[160:161], v[170:171], v[154:155]
	v_cvt_pk_bf16_f32 v154, v130, v131
	v_lshlrev_b64 v[130:131], 13, v[146:147]
	v_cvt_pk_bf16_f32 v155, v158, v159
	v_cvt_pk_bf16_f32 v157, v160, v161
	v_lshl_add_u64 v[130:131], v[134:135], 0, v[130:131]
	global_store_dwordx4 v[130:131], v[154:157], off
	v_pk_fma_f32 v[130:131], v[60:61], v[150:151], v[68:69]
	v_pk_fma_f32 v[146:147], v[56:57], v[162:163], v[64:65]
	v_pk_fma_f32 v[124:125], v[42:43], v[124:125], v[50:51]
	v_pk_fma_f32 v[150:151], v[26:27], v[166:167], v[48:49]
	v_pk_fma_f32 v[154:155], v[38:39], v[120:121], v[128:129]
	v_pk_fma_f32 v[160:161], v[16:17], v[110:111], v[118:119]
	s_waitcnt vmcnt(12)
	v_lshlrev_b32_e32 v118, 16, v106
	v_and_b32_e32 v119, 0xffff0000, v106
	v_pk_fma_f32 v[148:149], v[44:45], v[164:165], v[52:53]
	v_pk_fma_f32 v[162:163], v[40:41], v[126:127], v[130:131]
	v_pk_fma_f32 v[164:165], v[22:23], v[132:133], v[146:147]
	v_pk_fma_f32 v[158:159], v[28:29], v[116:117], v[124:125]
	v_pk_fma_f32 v[168:169], v[18:19], v[112:113], v[150:151]
	v_lshlrev_b32_e32 v124, 16, v107
	v_and_b32_e32 v125, 0xffff0000, v107
	s_waitcnt vmcnt(11)
	v_lshlrev_b32_e32 v146, 16, v104
	v_and_b32_e32 v147, 0xffff0000, v104
	v_lshlrev_b32_e32 v150, 16, v105
	v_and_b32_e32 v151, 0xffff0000, v105
	v_pk_fma_f32 v[104:105], v[12:13], v[118:119], v[154:155]
	v_pk_fma_f32 v[166:167], v[30:31], v[152:153], v[148:149]
	v_lshlrev_b32_e32 v128, 16, v102
	v_and_b32_e32 v129, 0xffff0000, v102
	v_lshlrev_b32_e32 v148, 16, v103
	v_and_b32_e32 v149, 0xffff0000, v103
	v_pk_fma_f32 v[102:103], v[14:15], v[124:125], v[162:163]
	v_mul_f32_e32 v162, 0x3d372713, v104
	v_mul_f32_e32 v163, 0x3d372713, v105
	v_mul_f32_e32 v162, v104, v162
	v_mul_f32_e32 v163, v105, v163
	v_fma_f32 v162, v104, v162, v104
	v_fma_f32 v163, v105, v163, v105
	v_mul_f32_e32 v162, 0x3f4c422a, v162
	v_mul_f32_e32 v163, 0x3f4c422a, v163
	v_mul_f32_e32 v162, -2.0, v162
	v_mul_f32_e32 v163, -2.0, v163
	v_mul_f32_e32 v162, 0x3fb8aa3b, v162
	v_mul_f32_e32 v163, 0x3fb8aa3b, v163
	v_exp_f32_e32 v162, v162
	v_exp_f32_e32 v163, v163
	v_pk_fma_f32 v[122:123], v[54:55], v[122:123], v[62:63]
	v_lshlrev_b32_e32 v130, 16, v109
	v_add_f32_e32 v162, 1.0, v162
	v_add_f32_e32 v163, 1.0, v163
	v_rcp_f32_e32 v162, v162
	v_rcp_f32_e32 v163, v163
	v_pk_fma_f32 v[156:157], v[20:21], v[114:115], v[122:123]
	v_lshlrev_b32_e32 v122, 16, v108
	v_and_b32_e32 v123, 0xffff0000, v108
	v_and_b32_e32 v131, 0xffff0000, v109
	v_pk_fma_f32 v[108:109], v[4:5], v[122:123], v[156:157]
	v_pk_fma_f32 v[156:157], v[8:9], v[128:129], v[158:159]
	v_pk_mul_f32 v[104:105], v[104:105], v[162:163]
	v_pk_fma_f32 v[154:155], v[10:11], v[148:149], v[166:167]
	v_pk_mul_f32 v[104:105], v[156:157], v[104:105]
	v_mul_f32_e32 v156, 0x3d372713, v102
	v_mul_f32_e32 v157, 0x3d372713, v103
	v_mul_f32_e32 v156, v102, v156
	v_mul_f32_e32 v157, v103, v157
	v_fma_f32 v156, v102, v156, v102
	v_fma_f32 v157, v103, v157, v103
	v_mul_f32_e32 v156, 0x3f4c422a, v156
	v_mul_f32_e32 v157, 0x3f4c422a, v157
	v_mul_f32_e32 v156, -2.0, v156
	v_mul_f32_e32 v157, -2.0, v157
	v_mul_f32_e32 v156, 0x3fb8aa3b, v156
	v_mul_f32_e32 v157, 0x3fb8aa3b, v157
	v_exp_f32_e32 v156, v156
	v_exp_f32_e32 v157, v157
	v_pk_fma_f32 v[106:107], v[6:7], v[130:131], v[164:165]
	v_pk_fma_f32 v[160:161], v[0:1], v[146:147], v[160:161]
	v_add_f32_e32 v156, 1.0, v156
	v_add_f32_e32 v157, 1.0, v157
	v_rcp_f32_e32 v156, v156
	v_rcp_f32_e32 v157, v157
	v_pk_fma_f32 v[158:159], v[2:3], v[150:151], v[168:169]
	v_pk_fma_f32 v[116:117], v[42:43], v[116:117], v[50:51]
	v_pk_fma_f32 v[112:113], v[26:27], v[112:113], v[48:49]
	v_pk_mul_f32 v[102:103], v[102:103], v[156:157]
	v_pk_fma_f32 v[110:111], v[24:25], v[110:111], v[46:47]
	v_pk_mul_f32 v[154:155], v[154:155], v[102:103]
	v_mul_f32_e32 v102, 0x3d372713, v108
	v_mul_f32_e32 v103, 0x3d372713, v109
	v_mul_f32_e32 v102, v108, v102
	v_mul_f32_e32 v103, v109, v103
	v_fma_f32 v102, v108, v102, v108
	v_fma_f32 v103, v109, v103, v109
	v_mul_f32_e32 v102, 0x3f4c422a, v102
	v_mul_f32_e32 v103, 0x3f4c422a, v103
	v_mul_f32_e32 v102, -2.0, v102
	v_mul_f32_e32 v103, -2.0, v103
	v_mul_f32_e32 v102, 0x3fb8aa3b, v102
	v_mul_f32_e32 v103, 0x3fb8aa3b, v103
	v_exp_f32_e32 v102, v102
	v_exp_f32_e32 v103, v103
	v_add_f32_e32 v102, 1.0, v102
	v_add_f32_e32 v103, 1.0, v103
	v_rcp_f32_e32 v102, v102
	v_rcp_f32_e32 v103, v103
	s_nop 0
	v_pk_mul_f32 v[102:103], v[108:109], v[102:103]
	s_nop 0
	v_pk_mul_f32 v[108:109], v[160:161], v[102:103]
	v_mul_f32_e32 v102, 0x3d372713, v106
	v_mul_f32_e32 v103, 0x3d372713, v107
	v_mul_f32_e32 v102, v106, v102
	v_mul_f32_e32 v103, v107, v103
	v_fma_f32 v102, v106, v102, v106
	v_fma_f32 v103, v107, v103, v107
	v_mul_f32_e32 v102, 0x3f4c422a, v102
	v_mul_f32_e32 v103, 0x3f4c422a, v103
	v_mul_f32_e32 v102, -2.0, v102
	v_mul_f32_e32 v103, -2.0, v103
	v_mul_f32_e32 v102, 0x3fb8aa3b, v102
	v_mul_f32_e32 v103, 0x3fb8aa3b, v103
	v_exp_f32_e32 v102, v102
	v_exp_f32_e32 v103, v103
	v_add_f32_e32 v102, 1.0, v102
	v_add_f32_e32 v103, 1.0, v103
	v_rcp_f32_e32 v102, v102
	v_rcp_f32_e32 v103, v103
	s_nop 0
	v_pk_mul_f32 v[102:103], v[106:107], v[102:103]
	s_nop 0
	v_pk_mul_f32 v[106:107], v[158:159], v[102:103]
	v_cvt_pk_bf16_f32 v102, v104, v105
	v_cvt_pk_bf16_f32 v105, v106, v107
	v_lshlrev_b64 v[106:107], 13, v[144:145]
	v_cvt_pk_bf16_f32 v103, v154, v155
	v_cvt_pk_bf16_f32 v104, v108, v109
	v_lshl_add_u64 v[106:107], v[134:135], 0, v[106:107]
	global_store_dwordx4 v[106:107], v[102:105], off
	v_pk_fma_f32 v[106:107], v[56:57], v[132:133], v[64:65]
	v_pk_fma_f32 v[108:109], v[54:55], v[114:115], v[62:63]
	v_pk_fma_f32 v[102:103], v[60:61], v[126:127], v[68:69]
	v_pk_fma_f32 v[104:105], v[58:59], v[120:121], v[66:67]
	v_pk_fma_f32 v[114:115], v[44:45], v[152:153], v[52:53]
	v_pk_fma_f32 v[120:121], v[38:39], v[118:119], v[104:105]
	v_pk_fma_f32 v[152:153], v[40:41], v[124:125], v[102:103]
	s_waitcnt vmcnt(11)
	v_lshlrev_b32_e32 v102, 16, v98
	v_and_b32_e32 v103, 0xffff0000, v98
	v_pk_fma_f32 v[154:155], v[22:23], v[130:131], v[106:107]
	v_pk_fma_f32 v[132:133], v[28:29], v[128:129], v[116:117]
	v_pk_fma_f32 v[158:159], v[18:19], v[150:151], v[112:113]
	v_lshlrev_b32_e32 v106, 16, v99
	v_and_b32_e32 v107, 0xffff0000, v99
	s_waitcnt vmcnt(10)
	v_lshlrev_b32_e32 v112, 16, v96
	v_and_b32_e32 v113, 0xffff0000, v96
	v_lshlrev_b32_e32 v116, 16, v97
	v_and_b32_e32 v117, 0xffff0000, v97
	v_pk_fma_f32 v[96:97], v[12:13], v[102:103], v[120:121]
	v_pk_fma_f32 v[126:127], v[20:21], v[122:123], v[108:109]
	v_pk_fma_f32 v[156:157], v[30:31], v[148:149], v[114:115]
	v_lshlrev_b32_e32 v108, 16, v94
	v_and_b32_e32 v109, 0xffff0000, v94
	v_lshlrev_b32_e32 v114, 16, v95
	v_and_b32_e32 v115, 0xffff0000, v95
	v_pk_fma_f32 v[94:95], v[14:15], v[106:107], v[152:153]
	v_mul_f32_e32 v152, 0x3d372713, v96
	v_mul_f32_e32 v153, 0x3d372713, v97
	v_mul_f32_e32 v152, v96, v152
	v_mul_f32_e32 v153, v97, v153
	v_fma_f32 v152, v96, v152, v96
	v_fma_f32 v153, v97, v153, v97
	v_mul_f32_e32 v152, 0x3f4c422a, v152
	v_mul_f32_e32 v153, 0x3f4c422a, v153
	v_mul_f32_e32 v152, -2.0, v152
	v_mul_f32_e32 v153, -2.0, v153
	v_mul_f32_e32 v152, 0x3fb8aa3b, v152
	v_mul_f32_e32 v153, 0x3fb8aa3b, v153
	v_exp_f32_e32 v152, v152
	v_exp_f32_e32 v153, v153
	v_lshlrev_b32_e32 v104, 16, v100
	v_and_b32_e32 v105, 0xffff0000, v100
	v_add_f32_e32 v152, 1.0, v152
	v_add_f32_e32 v153, 1.0, v153
	v_rcp_f32_e32 v152, v152
	v_rcp_f32_e32 v153, v153
	v_pk_fma_f32 v[144:145], v[16:17], v[146:147], v[110:111]
	v_lshlrev_b32_e32 v110, 16, v101
	v_and_b32_e32 v111, 0xffff0000, v101
	v_pk_fma_f32 v[100:101], v[4:5], v[104:105], v[126:127]
	v_pk_fma_f32 v[126:127], v[8:9], v[108:109], v[132:133]
	v_pk_mul_f32 v[96:97], v[96:97], v[152:153]
	v_pk_fma_f32 v[120:121], v[10:11], v[114:115], v[156:157]
	v_pk_mul_f32 v[96:97], v[126:127], v[96:97]
	v_mul_f32_e32 v126, 0x3d372713, v94
	v_mul_f32_e32 v127, 0x3d372713, v95
	v_mul_f32_e32 v126, v94, v126
	v_mul_f32_e32 v127, v95, v127
	v_fma_f32 v126, v94, v126, v94
	v_fma_f32 v127, v95, v127, v95
	v_mul_f32_e32 v126, 0x3f4c422a, v126
	v_mul_f32_e32 v127, 0x3f4c422a, v127
	v_mul_f32_e32 v126, -2.0, v126
	v_mul_f32_e32 v127, -2.0, v127
	v_mul_f32_e32 v126, 0x3fb8aa3b, v126
	v_mul_f32_e32 v127, 0x3fb8aa3b, v127
	v_exp_f32_e32 v126, v126
	v_exp_f32_e32 v127, v127
	v_pk_fma_f32 v[98:99], v[6:7], v[110:111], v[154:155]
	v_pk_fma_f32 v[144:145], v[0:1], v[112:113], v[144:145]
	v_add_f32_e32 v126, 1.0, v126
	v_add_f32_e32 v127, 1.0, v127
	v_rcp_f32_e32 v126, v126
	v_rcp_f32_e32 v127, v127
	v_pk_fma_f32 v[132:133], v[2:3], v[116:117], v[158:159]
	v_pk_mul_f32 v[94:95], v[94:95], v[126:127]
	s_nop 0
	v_pk_mul_f32 v[120:121], v[120:121], v[94:95]
	v_mul_f32_e32 v94, 0x3d372713, v100
	v_mul_f32_e32 v95, 0x3d372713, v101
	v_mul_f32_e32 v94, v100, v94
	v_mul_f32_e32 v95, v101, v95
	v_fma_f32 v94, v100, v94, v100
	v_fma_f32 v95, v101, v95, v101
	v_mul_f32_e32 v94, 0x3f4c422a, v94
	v_mul_f32_e32 v95, 0x3f4c422a, v95
	v_mul_f32_e32 v94, -2.0, v94
	v_mul_f32_e32 v95, -2.0, v95
	v_mul_f32_e32 v94, 0x3fb8aa3b, v94
	v_mul_f32_e32 v95, 0x3fb8aa3b, v95
	v_exp_f32_e32 v94, v94
	v_exp_f32_e32 v95, v95
	v_add_f32_e32 v94, 1.0, v94
	v_add_f32_e32 v95, 1.0, v95
	v_rcp_f32_e32 v94, v94
	v_rcp_f32_e32 v95, v95
	s_nop 0
	v_pk_mul_f32 v[94:95], v[100:101], v[94:95]
	s_nop 0
	v_pk_mul_f32 v[100:101], v[144:145], v[94:95]
	v_mul_f32_e32 v94, 0x3d372713, v98
	v_mul_f32_e32 v95, 0x3d372713, v99
	v_mul_f32_e32 v94, v98, v94
	v_mul_f32_e32 v95, v99, v95
	v_fma_f32 v94, v98, v94, v98
	v_fma_f32 v95, v99, v95, v99
	v_mul_f32_e32 v94, 0x3f4c422a, v94
	v_mul_f32_e32 v95, 0x3f4c422a, v95
	v_mul_f32_e32 v94, -2.0, v94
	v_mul_f32_e32 v95, -2.0, v95
	v_mul_f32_e32 v94, 0x3fb8aa3b, v94
	v_mul_f32_e32 v95, 0x3fb8aa3b, v95
	v_exp_f32_e32 v94, v94
	v_exp_f32_e32 v95, v95
	v_add_f32_e32 v94, 1.0, v94
	v_add_f32_e32 v95, 1.0, v95
	v_rcp_f32_e32 v94, v94
	v_rcp_f32_e32 v95, v95
	s_nop 0
	v_pk_mul_f32 v[94:95], v[98:99], v[94:95]
	s_nop 0
	v_pk_mul_f32 v[98:99], v[132:133], v[94:95]
	v_cvt_pk_bf16_f32 v94, v96, v97
	v_cvt_pk_bf16_f32 v97, v98, v99
	v_lshlrev_b64 v[98:99], 13, v[142:143]
	v_cvt_pk_bf16_f32 v95, v120, v121
	v_cvt_pk_bf16_f32 v96, v100, v101
	v_lshl_add_u64 v[98:99], v[134:135], 0, v[98:99]
	global_store_dwordx4 v[98:99], v[94:97], off
	v_pk_fma_f32 v[142:143], v[24:25], v[146:147], v[46:47]
	v_pk_fma_f32 v[98:99], v[56:57], v[130:131], v[64:65]
	v_pk_fma_f32 v[94:95], v[60:61], v[124:125], v[68:69]
	v_pk_fma_f32 v[96:97], v[58:59], v[118:119], v[66:67]
	v_pk_fma_f32 v[126:127], v[40:41], v[106:107], v[94:95]
	v_pk_fma_f32 v[118:119], v[38:39], v[102:103], v[96:97]
	s_waitcnt vmcnt(10)
	v_lshlrev_b32_e32 v94, 16, v90
	v_and_b32_e32 v95, 0xffff0000, v90
	v_pk_fma_f32 v[124:125], v[44:45], v[148:149], v[52:53]
	v_pk_fma_f32 v[118:119], v[12:13], v[94:95], v[118:119]
	v_pk_fma_f32 v[130:131], v[30:31], v[114:115], v[124:125]
	v_pk_fma_f32 v[124:125], v[16:17], v[112:113], v[142:143]
	v_mul_f32_e32 v142, 0x3d372713, v118
	v_mul_f32_e32 v143, 0x3d372713, v119
	v_mul_f32_e32 v142, v118, v142
	v_mul_f32_e32 v143, v119, v143
	v_fma_f32 v142, v118, v142, v118
	v_fma_f32 v143, v119, v143, v119
	v_mul_f32_e32 v142, 0x3f4c422a, v142
	v_mul_f32_e32 v143, 0x3f4c422a, v143
	v_mul_f32_e32 v142, -2.0, v142
	v_mul_f32_e32 v143, -2.0, v143
	v_mul_f32_e32 v142, 0x3fb8aa3b, v142
	v_mul_f32_e32 v143, 0x3fb8aa3b, v143
	v_exp_f32_e32 v142, v142
	v_exp_f32_e32 v143, v143
	v_pk_fma_f32 v[100:101], v[54:55], v[122:123], v[62:63]
	v_pk_fma_f32 v[122:123], v[42:43], v[128:129], v[50:51]
	v_add_f32_e32 v142, 1.0, v142
	v_add_f32_e32 v143, 1.0, v143
	v_rcp_f32_e32 v142, v142
	v_rcp_f32_e32 v143, v143
	v_pk_fma_f32 v[128:129], v[22:23], v[110:111], v[98:99]
	v_pk_fma_f32 v[122:123], v[28:29], v[108:109], v[122:123]
	v_lshlrev_b32_e32 v98, 16, v91
	v_and_b32_e32 v99, 0xffff0000, v91
	s_waitcnt vmcnt(9)
	v_lshlrev_b32_e32 v90, 16, v86
	v_and_b32_e32 v91, 0xffff0000, v86
	v_pk_fma_f32 v[126:127], v[14:15], v[98:99], v[126:127]
	v_pk_fma_f32 v[122:123], v[8:9], v[90:91], v[122:123]
	v_pk_mul_f32 v[118:119], v[118:119], v[142:143]
	v_pk_fma_f32 v[120:121], v[20:21], v[104:105], v[100:101]
	v_pk_mul_f32 v[118:119], v[122:123], v[118:119]
	v_mul_f32_e32 v122, 0x3d372713, v126
	v_mul_f32_e32 v123, 0x3d372713, v127
	v_mul_f32_e32 v122, v126, v122
	v_mul_f32_e32 v123, v127, v123
	v_fma_f32 v122, v126, v122, v126
	v_fma_f32 v123, v127, v123, v127
	v_mul_f32_e32 v122, 0x3f4c422a, v122
	v_mul_f32_e32 v123, 0x3f4c422a, v123
	v_mul_f32_e32 v122, -2.0, v122
	v_mul_f32_e32 v123, -2.0, v123
	v_mul_f32_e32 v122, 0x3fb8aa3b, v122
	v_mul_f32_e32 v123, 0x3fb8aa3b, v123
	v_exp_f32_e32 v122, v122
	v_exp_f32_e32 v123, v123
	v_lshlrev_b32_e32 v96, 16, v92
	v_and_b32_e32 v97, 0xffff0000, v92
	v_add_f32_e32 v122, 1.0, v122
	v_add_f32_e32 v123, 1.0, v123
	v_rcp_f32_e32 v122, v122
	v_rcp_f32_e32 v123, v123
	v_pk_fma_f32 v[120:121], v[4:5], v[96:97], v[120:121]
	v_lshlrev_b32_e32 v100, 16, v93
	v_and_b32_e32 v101, 0xffff0000, v93
	v_pk_mul_f32 v[122:123], v[126:127], v[122:123]
	v_mul_f32_e32 v126, 0x3d372713, v120
	v_mul_f32_e32 v127, 0x3d372713, v121
	v_mul_f32_e32 v126, v120, v126
	v_mul_f32_e32 v127, v121, v127
	v_fma_f32 v126, v120, v126, v120
	v_fma_f32 v127, v121, v127, v121
	v_mul_f32_e32 v126, 0x3f4c422a, v126
	v_mul_f32_e32 v127, 0x3f4c422a, v127
	v_mul_f32_e32 v126, -2.0, v126
	v_mul_f32_e32 v127, -2.0, v127
	v_mul_f32_e32 v126, 0x3fb8aa3b, v126
	v_mul_f32_e32 v127, 0x3fb8aa3b, v127
	v_exp_f32_e32 v126, v126
	v_exp_f32_e32 v127, v127
	v_lshlrev_b32_e32 v92, 16, v87
	v_and_b32_e32 v93, 0xffff0000, v87
	v_add_f32_e32 v126, 1.0, v126
	v_add_f32_e32 v127, 1.0, v127
	v_rcp_f32_e32 v126, v126
	v_rcp_f32_e32 v127, v127
	v_lshlrev_b32_e32 v86, 16, v88
	v_and_b32_e32 v87, 0xffff0000, v88
	v_pk_fma_f32 v[128:129], v[6:7], v[100:101], v[128:129]
	v_pk_fma_f32 v[124:125], v[0:1], v[86:87], v[124:125]
	v_pk_mul_f32 v[120:121], v[120:121], v[126:127]
	v_pk_fma_f32 v[132:133], v[26:27], v[150:151], v[48:49]
	v_pk_mul_f32 v[120:121], v[124:125], v[120:121]
	v_mul_f32_e32 v124, 0x3d372713, v128
	v_mul_f32_e32 v125, 0x3d372713, v129
	v_mul_f32_e32 v124, v128, v124
	v_mul_f32_e32 v125, v129, v125
	v_fma_f32 v124, v128, v124, v128
	v_fma_f32 v125, v129, v125, v129
	v_mul_f32_e32 v124, 0x3f4c422a, v124
	v_mul_f32_e32 v125, 0x3f4c422a, v125
	v_mul_f32_e32 v124, -2.0, v124
	v_mul_f32_e32 v125, -2.0, v125
	v_mul_f32_e32 v124, 0x3fb8aa3b, v124
	v_mul_f32_e32 v125, 0x3fb8aa3b, v125
	v_exp_f32_e32 v124, v124
	v_exp_f32_e32 v125, v125
	v_pk_fma_f32 v[132:133], v[18:19], v[116:117], v[132:133]
	v_lshlrev_b32_e32 v88, 16, v89
	v_add_f32_e32 v124, 1.0, v124
	v_add_f32_e32 v125, 1.0, v125
	v_rcp_f32_e32 v124, v124
	v_rcp_f32_e32 v125, v125
	v_and_b32_e32 v89, 0xffff0000, v89
	v_pk_fma_f32 v[130:131], v[10:11], v[92:93], v[130:131]
	v_pk_fma_f32 v[132:133], v[2:3], v[88:89], v[132:133]
	v_pk_mul_f32 v[122:123], v[130:131], v[122:123]
	v_pk_mul_f32 v[124:125], v[128:129], v[124:125]
	v_cvt_pk_bf16_f32 v118, v118, v119
	v_pk_mul_f32 v[124:125], v[132:133], v[124:125]
	v_cvt_pk_bf16_f32 v119, v122, v123
	v_lshlrev_b64 v[122:123], 13, v[140:141]
	v_cvt_pk_bf16_f32 v120, v120, v121
	v_cvt_pk_bf16_f32 v121, v124, v125
	v_lshl_add_u64 v[122:123], v[134:135], 0, v[122:123]
	v_pk_fma_f32 v[102:103], v[58:59], v[102:103], v[66:67]
	v_pk_fma_f32 v[108:109], v[42:43], v[108:109], v[50:51]
	global_store_dwordx4 v[122:123], v[118:121], off
	v_pk_fma_f32 v[112:113], v[24:25], v[112:113], v[46:47]
	v_pk_fma_f32 v[124:125], v[28:29], v[90:91], v[108:109]
	v_pk_fma_f32 v[118:119], v[38:39], v[94:95], v[102:103]
	s_waitcnt vmcnt(9)
	v_lshlrev_b32_e32 v102, 16, v82
	v_and_b32_e32 v103, 0xffff0000, v82
	s_waitcnt vmcnt(8)
	v_lshlrev_b32_e32 v108, 16, v80
	v_and_b32_e32 v109, 0xffff0000, v80
	v_pk_fma_f32 v[58:59], v[58:59], v[94:95], v[66:67]
	v_pk_fma_f32 v[24:25], v[24:25], v[86:87], v[46:47]
	v_pk_fma_f32 v[112:113], v[16:17], v[86:87], v[112:113]
	v_pk_fma_f32 v[38:39], v[38:39], v[102:103], v[58:59]
	v_pk_fma_f32 v[16:17], v[16:17], v[108:109], v[24:25]
	s_waitcnt vmcnt(6)
	v_lshlrev_b32_e32 v24, 16, v74
	v_and_b32_e32 v25, 0xffff0000, v74
	v_pk_fma_f32 v[118:119], v[12:13], v[102:103], v[118:119]
	v_pk_fma_f32 v[42:43], v[42:43], v[90:91], v[50:51]
	v_lshlrev_b32_e32 v50, 16, v72
	v_and_b32_e32 v51, 0xffff0000, v72
	v_pk_fma_f32 v[12:13], v[12:13], v[24:25], v[38:39]
	v_pk_fma_f32 v[112:113], v[0:1], v[108:109], v[112:113]
	v_mul_f32_e32 v126, 0x3d372713, v118
	v_mul_f32_e32 v127, 0x3d372713, v119
	v_pk_fma_f32 v[0:1], v[0:1], v[50:51], v[16:17]
	v_mul_f32_e32 v16, 0x3d372713, v12
	v_mul_f32_e32 v17, 0x3d372713, v13
	v_mul_f32_e32 v126, v118, v126
	v_mul_f32_e32 v127, v119, v127
	v_mul_f32_e32 v16, v12, v16
	v_mul_f32_e32 v17, v13, v17
	v_fma_f32 v126, v118, v126, v118
	v_fma_f32 v127, v119, v127, v119
	v_fma_f32 v16, v12, v16, v12
	v_fma_f32 v17, v13, v17, v13
	v_mul_f32_e32 v126, 0x3f4c422a, v126
	v_mul_f32_e32 v127, 0x3f4c422a, v127
	v_mul_f32_e32 v16, 0x3f4c422a, v16
	v_mul_f32_e32 v17, 0x3f4c422a, v17
	v_mul_f32_e32 v126, -2.0, v126
	v_mul_f32_e32 v127, -2.0, v127
	v_mul_f32_e32 v16, -2.0, v16
	v_mul_f32_e32 v17, -2.0, v17
	v_mul_f32_e32 v126, 0x3fb8aa3b, v126
	v_mul_f32_e32 v127, 0x3fb8aa3b, v127
	v_mul_f32_e32 v16, 0x3fb8aa3b, v16
	v_mul_f32_e32 v17, 0x3fb8aa3b, v17
	v_exp_f32_e32 v126, v126
	v_exp_f32_e32 v127, v127
	v_exp_f32_e32 v16, v16
	v_exp_f32_e32 v17, v17
	v_add_f32_e32 v126, 1.0, v126
	v_add_f32_e32 v127, 1.0, v127
	v_add_f32_e32 v16, 1.0, v16
	v_add_f32_e32 v17, 1.0, v17
	v_rcp_f32_e32 v126, v126
	v_rcp_f32_e32 v127, v127
	v_rcp_f32_e32 v16, v16
	v_rcp_f32_e32 v17, v17
	v_pk_fma_f32 v[106:107], v[60:61], v[106:107], v[68:69]
	v_pk_fma_f32 v[116:117], v[26:27], v[116:117], v[48:49]
	v_pk_fma_f32 v[120:121], v[40:41], v[98:99], v[106:107]
	v_lshlrev_b32_e32 v82, 16, v83
	v_and_b32_e32 v83, 0xffff0000, v83
	v_lshlrev_b32_e32 v106, 16, v78
	v_and_b32_e32 v107, 0xffff0000, v78
	v_lshlrev_b32_e32 v80, 16, v81
	v_and_b32_e32 v81, 0xffff0000, v81
	v_pk_fma_f32 v[60:61], v[60:61], v[98:99], v[68:69]
	v_pk_fma_f32 v[26:27], v[26:27], v[88:89], v[48:49]
	v_pk_fma_f32 v[116:117], v[18:19], v[88:89], v[116:117]
	v_pk_fma_f32 v[40:41], v[40:41], v[82:83], v[60:61]
	v_pk_fma_f32 v[28:29], v[28:29], v[106:107], v[42:43]
	v_pk_fma_f32 v[18:19], v[18:19], v[80:81], v[26:27]
	v_lshlrev_b32_e32 v26, 16, v75
	v_and_b32_e32 v27, 0xffff0000, v75
	v_lshlrev_b32_e32 v46, 16, v70
	v_and_b32_e32 v47, 0xffff0000, v70
	v_pk_fma_f32 v[120:121], v[14:15], v[82:83], v[120:121]
	v_pk_fma_f32 v[124:125], v[8:9], v[106:107], v[124:125]
	v_pk_mul_f32 v[118:119], v[118:119], v[126:127]
	v_pk_fma_f32 v[14:15], v[14:15], v[26:27], v[40:41]
	v_pk_fma_f32 v[8:9], v[8:9], v[46:47], v[28:29]
	v_pk_mul_f32 v[12:13], v[12:13], v[16:17]
	v_pk_mul_f32 v[118:119], v[124:125], v[118:119]
	v_mul_f32_e32 v124, 0x3d372713, v120
	v_mul_f32_e32 v125, 0x3d372713, v121
	v_pk_mul_f32 v[8:9], v[8:9], v[12:13]
	v_mul_f32_e32 v12, 0x3d372713, v14
	v_mul_f32_e32 v13, 0x3d372713, v15
	v_mul_f32_e32 v124, v120, v124
	v_mul_f32_e32 v125, v121, v125
	v_mul_f32_e32 v12, v14, v12
	v_mul_f32_e32 v13, v15, v13
	v_fma_f32 v124, v120, v124, v120
	v_fma_f32 v125, v121, v125, v121
	v_fma_f32 v12, v14, v12, v14
	v_fma_f32 v13, v15, v13, v15
	v_mul_f32_e32 v124, 0x3f4c422a, v124
	v_mul_f32_e32 v125, 0x3f4c422a, v125
	v_mul_f32_e32 v12, 0x3f4c422a, v12
	v_mul_f32_e32 v13, 0x3f4c422a, v13
	v_mul_f32_e32 v124, -2.0, v124
	v_mul_f32_e32 v125, -2.0, v125
	v_mul_f32_e32 v12, -2.0, v12
	v_mul_f32_e32 v13, -2.0, v13
	v_mul_f32_e32 v124, 0x3fb8aa3b, v124
	v_mul_f32_e32 v125, 0x3fb8aa3b, v125
	v_mul_f32_e32 v12, 0x3fb8aa3b, v12
	v_mul_f32_e32 v13, 0x3fb8aa3b, v13
	v_exp_f32_e32 v124, v124
	v_exp_f32_e32 v125, v125
	v_exp_f32_e32 v12, v12
	v_exp_f32_e32 v13, v13
	v_add_f32_e32 v124, 1.0, v124
	v_add_f32_e32 v125, 1.0, v125
	v_add_f32_e32 v12, 1.0, v12
	v_add_f32_e32 v13, 1.0, v13
	v_rcp_f32_e32 v124, v124
	v_rcp_f32_e32 v125, v125
	v_rcp_f32_e32 v12, v12
	v_rcp_f32_e32 v13, v13
	v_pk_fma_f32 v[104:105], v[54:55], v[104:105], v[62:63]
	v_pk_fma_f32 v[114:115], v[44:45], v[114:115], v[52:53]
	v_pk_fma_f32 v[122:123], v[20:21], v[96:97], v[104:105]
	v_lshlrev_b32_e32 v104, 16, v84
	v_and_b32_e32 v105, 0xffff0000, v84
	v_lshlrev_b32_e32 v78, 16, v79
	v_and_b32_e32 v79, 0xffff0000, v79
	v_pk_fma_f32 v[54:55], v[54:55], v[96:97], v[62:63]
	v_pk_fma_f32 v[44:45], v[44:45], v[92:93], v[52:53]
	v_pk_fma_f32 v[114:115], v[30:31], v[92:93], v[114:115]
	v_pk_fma_f32 v[20:21], v[20:21], v[104:105], v[54:55]
	v_pk_fma_f32 v[30:31], v[30:31], v[78:79], v[44:45]
	v_lshlrev_b32_e32 v42, 16, v76
	v_and_b32_e32 v43, 0xffff0000, v76
	v_lshlrev_b32_e32 v48, 16, v71
	v_and_b32_e32 v49, 0xffff0000, v71
	v_pk_fma_f32 v[122:123], v[4:5], v[104:105], v[122:123]
	v_pk_fma_f32 v[114:115], v[10:11], v[78:79], v[114:115]
	v_pk_mul_f32 v[120:121], v[120:121], v[124:125]
	v_pk_fma_f32 v[4:5], v[4:5], v[42:43], v[20:21]
	v_pk_fma_f32 v[10:11], v[10:11], v[48:49], v[30:31]
	v_pk_mul_f32 v[12:13], v[14:15], v[12:13]
	v_pk_mul_f32 v[114:115], v[114:115], v[120:121]
	v_mul_f32_e32 v120, 0x3d372713, v122
	v_mul_f32_e32 v121, 0x3d372713, v123
	v_pk_mul_f32 v[10:11], v[10:11], v[12:13]
	v_mul_f32_e32 v12, 0x3d372713, v4
	v_mul_f32_e32 v13, 0x3d372713, v5
	v_mul_f32_e32 v120, v122, v120
	v_mul_f32_e32 v121, v123, v121
	v_mul_f32_e32 v12, v4, v12
	v_mul_f32_e32 v13, v5, v13
	v_fma_f32 v120, v122, v120, v122
	v_fma_f32 v121, v123, v121, v123
	v_fma_f32 v12, v4, v12, v4
	v_fma_f32 v13, v5, v13, v5
	v_mul_f32_e32 v120, 0x3f4c422a, v120
	v_mul_f32_e32 v121, 0x3f4c422a, v121
	v_mul_f32_e32 v12, 0x3f4c422a, v12
	v_mul_f32_e32 v13, 0x3f4c422a, v13
	v_mul_f32_e32 v120, -2.0, v120
	v_mul_f32_e32 v121, -2.0, v121
	v_mul_f32_e32 v12, -2.0, v12
	v_mul_f32_e32 v13, -2.0, v13
	v_mul_f32_e32 v120, 0x3fb8aa3b, v120
	v_mul_f32_e32 v121, 0x3fb8aa3b, v121
	v_mul_f32_e32 v12, 0x3fb8aa3b, v12
	v_mul_f32_e32 v13, 0x3fb8aa3b, v13
	v_exp_f32_e32 v120, v120
	v_exp_f32_e32 v121, v121
	v_exp_f32_e32 v12, v12
	v_exp_f32_e32 v13, v13
	v_add_f32_e32 v120, 1.0, v120
	v_add_f32_e32 v121, 1.0, v121
	v_add_f32_e32 v12, 1.0, v12
	v_add_f32_e32 v13, 1.0, v13
	v_rcp_f32_e32 v120, v120
	v_rcp_f32_e32 v121, v121
	v_rcp_f32_e32 v12, v12
	v_rcp_f32_e32 v13, v13
	v_pk_fma_f32 v[110:111], v[56:57], v[110:111], v[64:65]
	v_lshlrev_b32_e32 v84, 16, v85
	v_and_b32_e32 v85, 0xffff0000, v85
	v_pk_fma_f32 v[56:57], v[56:57], v[100:101], v[64:65]
	v_pk_fma_f32 v[110:111], v[22:23], v[100:101], v[110:111]
	v_pk_fma_f32 v[22:23], v[22:23], v[84:85], v[56:57]
	v_lshlrev_b32_e32 v44, 16, v77
	v_and_b32_e32 v45, 0xffff0000, v77
	v_pk_fma_f32 v[110:111], v[6:7], v[84:85], v[110:111]
	v_pk_mul_f32 v[120:121], v[122:123], v[120:121]
	v_pk_fma_f32 v[6:7], v[6:7], v[44:45], v[22:23]
	v_pk_mul_f32 v[4:5], v[4:5], v[12:13]
	v_pk_mul_f32 v[112:113], v[112:113], v[120:121]
	v_mul_f32_e32 v120, 0x3d372713, v110
	v_mul_f32_e32 v121, 0x3d372713, v111
	v_pk_mul_f32 v[4:5], v[0:1], v[4:5]
	v_mul_f32_e32 v0, 0x3d372713, v6
	v_mul_f32_e32 v1, 0x3d372713, v7
	v_mul_f32_e32 v120, v110, v120
	v_mul_f32_e32 v121, v111, v121
	v_mul_f32_e32 v0, v6, v0
	v_mul_f32_e32 v1, v7, v1
	v_fma_f32 v120, v110, v120, v110
	v_fma_f32 v121, v111, v121, v111
	v_fma_f32 v0, v6, v0, v6
	v_fma_f32 v1, v7, v1, v7
	v_mul_f32_e32 v120, 0x3f4c422a, v120
	v_mul_f32_e32 v121, 0x3f4c422a, v121
	v_mul_f32_e32 v0, 0x3f4c422a, v0
	v_mul_f32_e32 v1, 0x3f4c422a, v1
	v_mul_f32_e32 v120, -2.0, v120
	v_mul_f32_e32 v121, -2.0, v121
	v_mul_f32_e32 v0, -2.0, v0
	v_mul_f32_e32 v1, -2.0, v1
	v_mul_f32_e32 v120, 0x3fb8aa3b, v120
	v_mul_f32_e32 v121, 0x3fb8aa3b, v121
	v_mul_f32_e32 v0, 0x3fb8aa3b, v0
	v_mul_f32_e32 v1, 0x3fb8aa3b, v1
	v_exp_f32_e32 v120, v120
	v_exp_f32_e32 v121, v121
	v_exp_f32_e32 v0, v0
	v_exp_f32_e32 v1, v1
	v_add_f32_e32 v120, 1.0, v120
	v_add_f32_e32 v121, 1.0, v121
	v_add_f32_e32 v0, 1.0, v0
	v_add_f32_e32 v1, 1.0, v1
	v_rcp_f32_e32 v120, v120
	v_rcp_f32_e32 v121, v121
	v_rcp_f32_e32 v0, v0
	v_rcp_f32_e32 v1, v1
	v_lshlrev_b32_e32 v52, 16, v73
	v_and_b32_e32 v53, 0xffff0000, v73
	v_pk_fma_f32 v[116:117], v[2:3], v[80:81], v[116:117]
	v_pk_mul_f32 v[110:111], v[110:111], v[120:121]
	v_pk_fma_f32 v[2:3], v[2:3], v[52:53], v[18:19]
	v_pk_mul_f32 v[0:1], v[6:7], v[0:1]
	v_pk_mul_f32 v[116:117], v[116:117], v[110:111]
	v_cvt_pk_bf16_f32 v111, v114, v115
	v_lshlrev_b64 v[114:115], 13, v[138:139]
	v_pk_mul_f32 v[6:7], v[2:3], v[0:1]
	v_cvt_pk_bf16_f32 v2, v4, v5
	v_lshlrev_b64 v[4:5], 13, v[136:137]
	v_cvt_pk_bf16_f32 v110, v118, v119
	v_cvt_pk_bf16_f32 v112, v112, v113
	v_cvt_pk_bf16_f32 v113, v116, v117
	v_lshl_add_u64 v[114:115], v[134:135], 0, v[114:115]
	v_cvt_pk_bf16_f32 v0, v8, v9
	v_cvt_pk_bf16_f32 v1, v10, v11
	v_cvt_pk_bf16_f32 v3, v6, v7
	v_lshl_add_u64 v[4:5], v[134:135], 0, v[4:5]
	global_store_dwordx4 v[114:115], v[110:113], off
	global_store_dwordx4 v[4:5], v[0:3], off
	s_andn2_b64 exec, exec, s[24:25]
	s_cbranch_execnz .LBB0_1907

.LBB0_1909:
	s_andn2_b64 vcc, exec, s[0:1]
	s_cbranch_vccnz .LBB0_1914
	s_and_saveexec_b64 s[10:11], s[34:35]
	s_cbranch_execz .LBB0_1913
	s_add_u32 s12, s8, 0x4000
	s_addc_u32 s13, s9, 0
	s_add_u32 s14, s6, 0x4000
	s_addc_u32 s15, s7, 0
	s_add_u32 s16, s6, 0x8000
	s_addc_u32 s17, s7, 0
	s_add_u32 s18, s6, 0xc000
	s_addc_u32 s19, s7, 0
	s_add_u32 s20, s6, 0x10000
	s_addc_u32 s21, s7, 0
	s_add_u32 s22, s6, 0x14000
	s_addc_u32 s23, s7, 0
	v_lshlrev_b32_e32 v194, 3, v32
	s_lshl_b32 s26, s71, 3
	s_mov_b64 s[24:25], 0
	s_add_u32 s100, s2, 0x2000
	s_addc_u32 s101, s3, 0
.LBB0_1912:
	v_ashrrev_i32_e32 v0, 31, v32
	v_lshrrev_b32_e32 v0, 23, v0
	v_add_u32_e32 v0, v32, v0
	v_ashrrev_i32_e32 v0, 9, v0
	v_mul_i32_i24_e32 v1, 0x200, v0
	v_lshlrev_b32_e32 v1, 3, v1
	v_sub_u32_e32 v134, v194, v1
	v_lshlrev_b32_e32 v150, 3, v0
	v_ashrrev_i32_e32 v135, 31, v134
	v_and_b32_e32 v224, 0xff8, v150
	v_lshlrev_b64 v[42:43], 2, v[134:135]
	v_cmp_eq_u32_e32 vcc, 0, v224
	v_lshl_add_u64 v[0:1], s[6:7], 0, v[42:43]
	global_load_dwordx4 v[54:57], v[0:1], off offset:16
	global_load_dwordx4 v[58:61], v[0:1], off
	v_lshl_add_u64 v[0:1], s[14:15], 0, v[42:43]
	global_load_dwordx4 v[24:27], v[0:1], off offset:16
	global_load_dwordx4 v[46:49], v[0:1], off
	v_lshl_add_u64 v[0:1], s[16:17], 0, v[42:43]
	global_load_dwordx4 v[20:23], v[0:1], off offset:16
	global_load_dwordx4 v[38:41], v[0:1], off
	v_lshl_add_u64 v[0:1], s[18:19], 0, v[42:43]
	global_load_dwordx4 v[16:19], v[0:1], off offset:16
	global_load_dwordx4 v[28:31], v[0:1], off
	v_lshl_add_u64 v[0:1], s[20:21], 0, v[42:43]
	v_lshl_add_u64 v[8:9], s[22:23], 0, v[42:43]
	v_lshl_add_u64 v[44:45], s[8:9], 0, v[42:43]
	v_lshl_add_u64 v[50:51], s[12:13], 0, v[42:43]
	s_waitcnt lgkmcnt(0)
	global_load_dwordx4 v[4:7], v[0:1], off offset:16
	global_load_dwordx4 v[12:15], v[0:1], off
	s_nop 0
	global_load_dwordx4 v[0:3], v[8:9], off offset:16
	s_nop 0
	global_load_dwordx4 v[8:11], v[8:9], off
	s_nop 0
	global_load_dwordx4 v[62:65], v[44:45], off offset:16
	global_load_dwordx4 v[66:69], v[44:45], off
	s_nop 0
	global_load_dwordx4 v[42:45], v[50:51], off offset:16
	s_nop 0
	global_load_dwordx4 v[50:53], v[50:51], off
	v_ashrrev_i32_e32 v151, 31, v150
	v_cndmask_b32_e64 v213, 2, 0, vcc
	v_lshlrev_b32_e32 v212, 1, v134
	v_lshl_add_u32 v212, v150, 14, v212
	v_lshlrev_b32_e32 v214, 13, v213
	v_lshlrev_b32_e32 v213, 14, v213
	v_sub_u32_e32 v213, v212, v213
	v_sub_u32_e32 v214, v212, v214
	global_load_dwordx4 v[216:219], v213, s[2:3]
	global_load_dwordx4 v[220:223], v213, s[100:101]
	global_load_dwordx4 v[200:203], v214, s[2:3]
	global_load_dwordx4 v[208:211], v214, s[100:101]
	global_load_dwordx4 v[130:133], v212, s[2:3]
	global_load_dwordx4 v[126:129], v212, s[100:101]
	v_add_u32_e32 v213, 0x4000, v212
	global_load_dwordx4 v[122:125], v213, s[2:3]
	global_load_dwordx4 v[118:121], v213, s[100:101]
	v_add_u32_e32 v214, 0x8000, v212
	global_load_dwordx4 v[114:117], v214, s[2:3]
	global_load_dwordx4 v[110:113], v214, s[100:101]
	v_add_u32_e32 v213, 0xc000, v212
	global_load_dwordx4 v[106:109], v213, s[2:3]
	global_load_dwordx4 v[102:105], v213, s[100:101]
	v_add_u32_e32 v214, 0x10000, v212
	global_load_dwordx4 v[98:101], v214, s[2:3]
	global_load_dwordx4 v[94:97], v214, s[100:101]
	v_add_u32_e32 v213, 0x14000, v212
	global_load_dwordx4 v[90:93], v213, s[2:3]
	global_load_dwordx4 v[86:89], v213, s[100:101]
	v_add_u32_e32 v214, 0x18000, v212
	global_load_dwordx4 v[82:85], v214, s[2:3]
	global_load_dwordx4 v[78:81], v214, s[100:101]
	v_add_u32_e32 v213, 0x1c000, v212
	global_load_dwordx4 v[70:73], v213, s[100:101]
	global_load_dwordx4 v[74:77], v213, s[2:3]
	v_or_b32_e32 v148, 1, v150
	s_nop 0
	v_ashrrev_i32_e32 v149, 31, v148
	v_or_b32_e32 v146, 2, v150
	v_ashrrev_i32_e32 v147, 31, v146
	v_or_b32_e32 v144, 3, v150
	v_ashrrev_i32_e32 v145, 31, v144
	v_or_b32_e32 v142, 4, v150
	v_ashrrev_i32_e32 v143, 31, v142
	v_or_b32_e32 v140, 5, v150
	v_ashrrev_i32_e32 v141, 31, v140
	v_or_b32_e32 v138, 6, v150
	v_ashrrev_i32_e32 v139, 31, v138
	v_or_b32_e32 v136, 7, v150
	v_ashrrev_i32_e32 v137, 31, v136
	v_lshl_add_u64 v[134:135], s[4:5], 0, v[134:135]
	v_add_u32_e32 v32, s71, v32
	v_add_u32_e32 v194, s26, v194
	s_waitcnt vmcnt(19)
	v_cndmask_b32_e64 v161, v219, 0, vcc
	v_cndmask_b32_e64 v164, v218, 0, vcc
	v_cndmask_b32_e64 v166, v217, 0, vcc
	v_cndmask_b32_e64 v167, v216, 0, vcc
	v_lshlrev_b32_e32 v168, 16, v167
	v_and_b32_e32 v169, 0xffff0000, v167
	s_waitcnt vmcnt(18)
	v_cndmask_b32_e64 v156, v223, 0, vcc
	v_cndmask_b32_e64 v159, v222, 0, vcc
	v_cndmask_b32_e64 v162, v221, 0, vcc
	v_cndmask_b32_e64 v165, v220, 0, vcc
	v_cmp_ne_u32_e32 vcc, 0, v224
	v_lshlrev_b32_e32 v170, 16, v166
	v_and_b32_e32 v171, 0xffff0000, v166
	v_lshlrev_b32_e32 v166, 16, v164
	s_nop 0
	v_and_b32_e32 v167, 0xffff0000, v164
	v_lshlrev_b32_e32 v172, 16, v161
	v_and_b32_e32 v173, 0xffff0000, v161
	v_lshlrev_b32_e32 v164, 16, v165
	v_and_b32_e32 v165, 0xffff0000, v165
	v_lshlrev_b32_e32 v174, 16, v162
	v_and_b32_e32 v175, 0xffff0000, v162
	v_lshlrev_b32_e32 v176, 16, v159
	v_and_b32_e32 v177, 0xffff0000, v159
	v_lshlrev_b32_e32 v178, 16, v156
	v_and_b32_e32 v179, 0xffff0000, v156
	v_pk_fma_f32 v[182:183], v[58:59], v[168:169], v[66:67]
	v_pk_fma_f32 v[180:181], v[60:61], v[170:171], v[68:69]
	v_pk_fma_f32 v[184:185], v[56:57], v[172:173], v[64:65]
	v_pk_fma_f32 v[188:189], v[54:55], v[166:167], v[62:63]
	v_pk_fma_f32 v[190:191], v[48:49], v[174:175], v[52:53]
	v_pk_fma_f32 v[192:193], v[46:47], v[164:165], v[50:51]
	v_pk_fma_f32 v[196:197], v[26:27], v[178:179], v[44:45]
	v_pk_fma_f32 v[198:199], v[24:25], v[176:177], v[42:43]
	s_waitcnt vmcnt(17)
	v_cndmask_b32_e32 v160, 0, v201, vcc
	v_cndmask_b32_e32 v163, 0, v200, vcc
	v_cndmask_b32_e32 v154, 0, v203, vcc
	v_cndmask_b32_e32 v157, 0, v202, vcc
	s_waitcnt vmcnt(16)
	v_cndmask_b32_e32 v152, 0, v211, vcc
	v_cndmask_b32_e32 v153, 0, v210, vcc
	v_cndmask_b32_e32 v155, 0, v209, vcc
	v_cndmask_b32_e32 v158, 0, v208, vcc
	v_lshlrev_b32_e32 v162, 16, v163
	s_nop 0
	v_and_b32_e32 v163, 0xffff0000, v163
	v_lshlrev_b32_e32 v166, 16, v160
	v_and_b32_e32 v167, 0xffff0000, v160
	v_lshlrev_b32_e32 v164, 16, v157
	v_and_b32_e32 v165, 0xffff0000, v157
	v_lshlrev_b32_e32 v170, 16, v154
	v_and_b32_e32 v171, 0xffff0000, v154
	v_lshlrev_b32_e32 v168, 16, v158
	v_and_b32_e32 v169, 0xffff0000, v158
	v_lshlrev_b32_e32 v174, 16, v155
	v_and_b32_e32 v175, 0xffff0000, v155
	v_lshlrev_b32_e32 v172, 16, v153
	v_and_b32_e32 v173, 0xffff0000, v153
	v_lshlrev_b32_e32 v176, 16, v152
	v_and_b32_e32 v177, 0xffff0000, v152
	v_pk_fma_f32 v[178:179], v[38:39], v[162:163], v[182:183]
	v_pk_fma_f32 v[186:187], v[40:41], v[166:167], v[180:181]
	v_pk_fma_f32 v[180:181], v[20:21], v[164:165], v[188:189]
	v_pk_fma_f32 v[188:189], v[22:23], v[170:171], v[184:185]
	v_pk_fma_f32 v[182:183], v[28:29], v[168:169], v[192:193]
	v_pk_fma_f32 v[190:191], v[30:31], v[174:175], v[190:191]
	v_pk_fma_f32 v[192:193], v[18:19], v[176:177], v[196:197]
	v_pk_fma_f32 v[184:185], v[16:17], v[172:173], v[198:199]
	s_nop 0
	v_lshlrev_b64 v[150:151], 12, v[150:151]
	s_nop 0
	v_lshl_add_u64 v[150:151], v[134:135], 0, v[150:151]
	s_nop 0
	v_pk_fma_f32 v[164:165], v[54:55], v[164:165], v[62:63]
	s_nop 0
	v_lshlrev_b64 v[148:149], 12, v[148:149]
	s_nop 0
	s_waitcnt vmcnt(15)
	v_lshlrev_b32_e32 v152, 16, v130
	v_and_b32_e32 v153, 0xffff0000, v130
	v_lshlrev_b32_e32 v154, 16, v131
	v_and_b32_e32 v155, 0xffff0000, v131
	v_lshlrev_b32_e32 v156, 16, v133
	v_and_b32_e32 v157, 0xffff0000, v133
	v_pk_fma_f32 v[178:179], v[12:13], v[152:153], v[178:179]
	v_lshlrev_b32_e32 v130, 16, v132
	v_and_b32_e32 v131, 0xffff0000, v132
	v_pk_fma_f32 v[180:181], v[4:5], v[130:131], v[180:181]
	s_waitcnt vmcnt(14)
	v_lshlrev_b32_e32 v158, 16, v127
	v_and_b32_e32 v159, 0xffff0000, v127
	v_lshlrev_b32_e32 v160, 16, v129
	v_and_b32_e32 v161, 0xffff0000, v129
	v_lshlrev_b32_e32 v132, 16, v126
	v_and_b32_e32 v133, 0xffff0000, v126
	v_lshlrev_b32_e32 v126, 16, v128
	v_and_b32_e32 v127, 0xffff0000, v128
	v_pk_fma_f32 v[128:129], v[14:15], v[154:155], v[186:187]
	v_pk_fma_f32 v[186:187], v[6:7], v[156:157], v[188:189]
	v_pk_fma_f32 v[188:189], v[10:11], v[158:159], v[190:191]
	v_pk_fma_f32 v[190:191], v[2:3], v[160:161], v[192:193]
	v_mul_f32_e32 v192, 0x3d372713, v178
	v_mul_f32_e32 v192, v178, v192
	v_fma_f32 v192, v178, v192, v178
	v_mul_f32_e32 v192, 0x3f4c422a, v192
	v_mul_f32_e32 v192, -2.0, v192
	v_mul_f32_e32 v192, 0x3fb8aa3b, v192
	v_exp_f32_e32 v192, v192
	v_pk_fma_f32 v[182:183], v[8:9], v[132:133], v[182:183]
	v_pk_fma_f32 v[184:185], v[0:1], v[126:127], v[184:185]
	v_add_f32_e32 v192, 1.0, v192
	v_rcp_f32_e32 v192, v192
	v_lshl_add_u64 v[148:149], v[134:135], 0, v[148:149]
	v_mul_f32_e32 v178, v178, v192
	v_mul_f32_e32 v178, v182, v178
	v_mul_f32_e32 v182, 0x3d372713, v179
	v_mul_f32_e32 v182, v179, v182
	v_fma_f32 v182, v179, v182, v179
	v_mul_f32_e32 v182, 0x3f4c422a, v182
	v_mul_f32_e32 v182, -2.0, v182
	v_mul_f32_e32 v182, 0x3fb8aa3b, v182
	v_exp_f32_e32 v182, v182
	s_nop 0
	v_add_f32_e32 v182, 1.0, v182
	v_rcp_f32_e32 v182, v182
	s_nop 0
	v_mul_f32_e32 v179, v179, v182
	v_mul_f32_e32 v182, 0x3d372713, v128
	v_mul_f32_e32 v182, v128, v182
	v_fma_f32 v182, v128, v182, v128
	v_mul_f32_e32 v182, 0x3f4c422a, v182
	v_mul_f32_e32 v182, -2.0, v182
	v_mul_f32_e32 v182, 0x3fb8aa3b, v182
	v_exp_f32_e32 v182, v182
	v_mul_f32_e32 v179, v183, v179
	v_add_f32_e32 v182, 1.0, v182
	v_rcp_f32_e32 v182, v182
	s_nop 0
	v_lshlrev_b64 v[146:147], 12, v[146:147]
	v_lshl_add_u64 v[146:147], v[134:135], 0, v[146:147]
	v_mul_f32_e32 v128, v128, v182
	v_mul_f32_e32 v182, v188, v128
	v_mul_f32_e32 v128, 0x3d372713, v129
	v_mul_f32_e32 v128, v129, v128
	v_fma_f32 v128, v129, v128, v129
	v_mul_f32_e32 v128, 0x3f4c422a, v128
	v_mul_f32_e32 v128, -2.0, v128
	v_mul_f32_e32 v128, 0x3fb8aa3b, v128
	v_exp_f32_e32 v128, v128
	v_cmp_lt_i32_e32 vcc, s79, v32
	s_or_b64 s[24:25], vcc, s[24:25]
	v_add_f32_e32 v128, 1.0, v128
	v_rcp_f32_e32 v128, v128
	s_nop 0
	v_mul_f32_e32 v128, v129, v128
	v_mul_f32_e32 v129, v189, v128
	v_mul_f32_e32 v128, 0x3d372713, v180
	v_mul_f32_e32 v128, v180, v128
	v_fma_f32 v128, v180, v128, v180
	v_mul_f32_e32 v128, 0x3f4c422a, v128
	v_mul_f32_e32 v128, -2.0, v128
	v_mul_f32_e32 v128, 0x3fb8aa3b, v128
	v_exp_f32_e32 v128, v128
	s_nop 0
	v_add_f32_e32 v128, 1.0, v128
	v_rcp_f32_e32 v128, v128
	s_nop 0
	v_mul_f32_e32 v128, v180, v128
	v_mul_f32_e32 v180, v184, v128
	v_mul_f32_e32 v128, 0x3d372713, v181
	v_mul_f32_e32 v128, v181, v128
	v_fma_f32 v128, v181, v128, v181
	v_mul_f32_e32 v128, 0x3f4c422a, v128
	v_mul_f32_e32 v128, -2.0, v128
	v_mul_f32_e32 v128, 0x3fb8aa3b, v128
	v_exp_f32_e32 v128, v128
	s_nop 0
	v_add_f32_e32 v128, 1.0, v128
	v_rcp_f32_e32 v128, v128
	s_nop 0
	v_mul_f32_e32 v128, v181, v128
	v_mul_f32_e32 v181, v185, v128
	v_mul_f32_e32 v128, 0x3d372713, v186
	v_mul_f32_e32 v128, v186, v128
	v_fma_f32 v128, v186, v128, v186
	v_mul_f32_e32 v128, 0x3f4c422a, v128
	v_mul_f32_e32 v128, -2.0, v128
	v_mul_f32_e32 v128, 0x3fb8aa3b, v128
	v_exp_f32_e32 v128, v128
	s_nop 0
	v_add_f32_e32 v128, 1.0, v128
	v_rcp_f32_e32 v128, v128
	s_nop 0
	v_mul_f32_e32 v128, v186, v128
	v_mul_f32_e32 v183, v190, v128
	v_mul_f32_e32 v128, 0x3d372713, v187
	v_mul_f32_e32 v128, v187, v128
	v_fma_f32 v128, v187, v128, v187
	v_mul_f32_e32 v128, 0x3f4c422a, v128
	v_mul_f32_e32 v128, -2.0, v128
	v_mul_f32_e32 v128, 0x3fb8aa3b, v128
	v_exp_f32_e32 v128, v128
	s_nop 0
	v_add_f32_e32 v128, 1.0, v128
	v_rcp_f32_e32 v128, v128
	s_nop 0
	v_mul_f32_e32 v128, v187, v128
	v_mul_f32_e32 v184, v191, v128
	v_mov_b32_e32 v128, v33
	v_cvt_pk_fp8_f32 v128, v178, v179
	v_cvt_pk_fp8_f32 v128, v182, v129 op_sel:[0,0,1]
	v_mov_b32_e32 v129, v33
	v_cvt_pk_fp8_f32 v129, v180, v181
	v_cvt_pk_fp8_f32 v129, v183, v184 op_sel:[0,0,1]
	v_pk_fma_f32 v[182:183], v[26:27], v[176:177], v[44:45]
	v_pk_fma_f32 v[184:185], v[24:25], v[172:173], v[42:43]
	v_pk_fma_f32 v[182:183], v[18:19], v[160:161], v[182:183]
	global_store_dwordx2 v[150:151], v[128:129], off
	v_pk_fma_f32 v[128:129], v[60:61], v[166:167], v[68:69]
	v_pk_fma_f32 v[150:151], v[58:59], v[162:163], v[66:67]
	v_pk_fma_f32 v[162:163], v[56:57], v[170:171], v[64:65]
	v_pk_fma_f32 v[166:167], v[48:49], v[174:175], v[52:53]
	v_pk_fma_f32 v[174:175], v[46:47], v[168:169], v[50:51]
	v_pk_fma_f32 v[168:169], v[38:39], v[152:153], v[150:151]
	v_pk_fma_f32 v[176:177], v[40:41], v[154:155], v[128:129]
	s_waitcnt vmcnt(14)
	v_lshlrev_b32_e32 v128, 16, v122
	v_and_b32_e32 v129, 0xffff0000, v122
	v_pk_fma_f32 v[170:171], v[20:21], v[130:131], v[164:165]
	v_pk_fma_f32 v[178:179], v[22:23], v[156:157], v[162:163]
	v_pk_fma_f32 v[180:181], v[30:31], v[158:159], v[166:167]
	v_lshlrev_b32_e32 v150, 16, v123
	v_and_b32_e32 v151, 0xffff0000, v123
	v_lshlrev_b32_e32 v162, 16, v125
	v_and_b32_e32 v163, 0xffff0000, v125
	s_waitcnt vmcnt(13)
	v_lshlrev_b32_e32 v164, 16, v119
	v_and_b32_e32 v165, 0xffff0000, v119
	v_lshlrev_b32_e32 v166, 16, v121
	v_and_b32_e32 v167, 0xffff0000, v121
	v_pk_fma_f32 v[168:169], v[12:13], v[128:129], v[168:169]
	v_lshlrev_b32_e32 v122, 16, v124
	v_and_b32_e32 v123, 0xffff0000, v124
	v_lshlrev_b32_e32 v124, 16, v118
	v_and_b32_e32 v125, 0xffff0000, v118
	v_lshlrev_b32_e32 v118, 16, v120
	v_and_b32_e32 v119, 0xffff0000, v120
	v_pk_fma_f32 v[120:121], v[14:15], v[150:151], v[176:177]
	v_pk_fma_f32 v[176:177], v[6:7], v[162:163], v[178:179]
	v_pk_fma_f32 v[178:179], v[10:11], v[164:165], v[180:181]
	v_pk_fma_f32 v[180:181], v[2:3], v[166:167], v[182:183]
	v_mul_f32_e32 v182, 0x3d372713, v168
	v_mul_f32_e32 v182, v168, v182
	v_fma_f32 v182, v168, v182, v168
	v_mul_f32_e32 v182, 0x3f4c422a, v182
	v_mul_f32_e32 v182, -2.0, v182
	v_mul_f32_e32 v182, 0x3fb8aa3b, v182
	v_exp_f32_e32 v182, v182
	v_pk_fma_f32 v[172:173], v[28:29], v[132:133], v[174:175]
	v_pk_fma_f32 v[170:171], v[4:5], v[122:123], v[170:171]
	v_pk_fma_f32 v[172:173], v[8:9], v[124:125], v[172:173]
	v_add_f32_e32 v182, 1.0, v182
	v_rcp_f32_e32 v182, v182
	v_pk_fma_f32 v[174:175], v[16:17], v[126:127], v[184:185]
	v_pk_fma_f32 v[132:133], v[46:47], v[132:133], v[50:51]
	v_pk_fma_f32 v[174:175], v[0:1], v[118:119], v[174:175]
	v_mul_f32_e32 v168, v168, v182
	v_mul_f32_e32 v168, v172, v168
	v_mul_f32_e32 v172, 0x3d372713, v169
	v_mul_f32_e32 v172, v169, v172
	v_fma_f32 v172, v169, v172, v169
	v_mul_f32_e32 v172, 0x3f4c422a, v172
	v_mul_f32_e32 v172, -2.0, v172
	v_mul_f32_e32 v172, 0x3fb8aa3b, v172
	v_exp_f32_e32 v172, v172
	v_pk_fma_f32 v[126:127], v[24:25], v[126:127], v[42:43]
	v_add_f32_e32 v172, 1.0, v172
	v_rcp_f32_e32 v172, v172
	s_nop 0
	v_mul_f32_e32 v169, v169, v172
	v_mul_f32_e32 v172, 0x3d372713, v120
	v_mul_f32_e32 v172, v120, v172
	v_fma_f32 v172, v120, v172, v120
	v_mul_f32_e32 v172, 0x3f4c422a, v172
	v_mul_f32_e32 v172, -2.0, v172
	v_mul_f32_e32 v172, 0x3fb8aa3b, v172
	v_exp_f32_e32 v172, v172
	v_mul_f32_e32 v169, v173, v169
	v_add_f32_e32 v172, 1.0, v172
	v_rcp_f32_e32 v172, v172
	s_nop 0
	v_mul_f32_e32 v120, v120, v172
	v_mul_f32_e32 v172, v178, v120
	v_mul_f32_e32 v120, 0x3d372713, v121
	v_mul_f32_e32 v120, v121, v120
	v_fma_f32 v120, v121, v120, v121
	v_mul_f32_e32 v120, 0x3f4c422a, v120
	v_mul_f32_e32 v120, -2.0, v120
	v_mul_f32_e32 v120, 0x3fb8aa3b, v120
	v_exp_f32_e32 v120, v120
	s_nop 0
	v_add_f32_e32 v120, 1.0, v120
	v_rcp_f32_e32 v120, v120
	s_nop 0
	v_mul_f32_e32 v120, v121, v120
	v_mul_f32_e32 v121, v179, v120
	v_mul_f32_e32 v120, 0x3d372713, v170
	v_mul_f32_e32 v120, v170, v120
	v_fma_f32 v120, v170, v120, v170
	v_mul_f32_e32 v120, 0x3f4c422a, v120
	v_mul_f32_e32 v120, -2.0, v120
	v_mul_f32_e32 v120, 0x3fb8aa3b, v120
	v_exp_f32_e32 v120, v120
	s_nop 0
	v_add_f32_e32 v120, 1.0, v120
	v_rcp_f32_e32 v120, v120
	s_nop 0
	v_mul_f32_e32 v120, v170, v120
	v_mul_f32_e32 v170, v174, v120
	v_mul_f32_e32 v120, 0x3d372713, v171
	v_mul_f32_e32 v120, v171, v120
	v_fma_f32 v120, v171, v120, v171
	v_mul_f32_e32 v120, 0x3f4c422a, v120
	v_mul_f32_e32 v120, -2.0, v120
	v_mul_f32_e32 v120, 0x3fb8aa3b, v120
	v_exp_f32_e32 v120, v120
	s_nop 0
	v_add_f32_e32 v120, 1.0, v120
	v_rcp_f32_e32 v120, v120
	s_nop 0
	v_mul_f32_e32 v120, v171, v120
	v_mul_f32_e32 v171, v175, v120
	v_mul_f32_e32 v120, 0x3d372713, v176
	v_mul_f32_e32 v120, v176, v120
	v_fma_f32 v120, v176, v120, v176
	v_mul_f32_e32 v120, 0x3f4c422a, v120
	v_mul_f32_e32 v120, -2.0, v120
	v_mul_f32_e32 v120, 0x3fb8aa3b, v120
	v_exp_f32_e32 v120, v120
	s_nop 0
	v_add_f32_e32 v120, 1.0, v120
	v_rcp_f32_e32 v120, v120
	s_nop 0
	v_mul_f32_e32 v120, v176, v120
	v_mul_f32_e32 v173, v180, v120
	v_mul_f32_e32 v120, 0x3d372713, v177
	v_mul_f32_e32 v120, v177, v120
	v_fma_f32 v120, v177, v120, v177
	v_mul_f32_e32 v120, 0x3f4c422a, v120
	v_mul_f32_e32 v120, -2.0, v120
	v_mul_f32_e32 v120, 0x3fb8aa3b, v120
	v_exp_f32_e32 v120, v120
	s_nop 0
	v_add_f32_e32 v120, 1.0, v120
	v_rcp_f32_e32 v120, v120
	s_nop 0
	v_mul_f32_e32 v120, v177, v120
	v_mul_f32_e32 v174, v181, v120
	v_mov_b32_e32 v120, v33
	v_cvt_pk_fp8_f32 v120, v168, v169
	v_cvt_pk_fp8_f32 v120, v172, v121 op_sel:[0,0,1]
	v_mov_b32_e32 v121, v33
	v_cvt_pk_fp8_f32 v121, v170, v171
	v_pk_fma_f32 v[170:171], v[26:27], v[160:161], v[44:45]
	v_cvt_pk_fp8_f32 v121, v173, v174 op_sel:[0,0,1]
	v_pk_fma_f32 v[170:171], v[18:19], v[166:167], v[170:171]
	global_store_dwordx2 v[148:149], v[120:121], off
	v_pk_fma_f32 v[120:121], v[60:61], v[154:155], v[68:69]
	v_pk_fma_f32 v[148:149], v[58:59], v[152:153], v[66:67]
	v_pk_fma_f32 v[152:153], v[56:57], v[156:157], v[64:65]
	v_pk_fma_f32 v[154:155], v[54:55], v[130:131], v[62:63]
	v_pk_fma_f32 v[156:157], v[48:49], v[158:159], v[52:53]
	v_pk_fma_f32 v[130:131], v[38:39], v[128:129], v[148:149]
	v_pk_fma_f32 v[158:159], v[40:41], v[150:151], v[120:121]
	s_waitcnt vmcnt(13)
	v_lshlrev_b32_e32 v120, 16, v114
	v_and_b32_e32 v121, 0xffff0000, v114
	v_pk_fma_f32 v[130:131], v[12:13], v[120:121], v[130:131]
	v_pk_fma_f32 v[148:149], v[20:21], v[122:123], v[154:155]
	v_mul_f32_e32 v172, 0x3d372713, v130
	v_mul_f32_e32 v172, v130, v172
	v_fma_f32 v172, v130, v172, v130
	v_mul_f32_e32 v172, 0x3f4c422a, v172
	v_mul_f32_e32 v172, -2.0, v172
	v_mul_f32_e32 v172, 0x3fb8aa3b, v172
	v_exp_f32_e32 v172, v172
	v_pk_fma_f32 v[154:155], v[28:29], v[124:125], v[132:133]
	v_pk_fma_f32 v[168:169], v[30:31], v[164:165], v[156:157]
	v_pk_fma_f32 v[156:157], v[16:17], v[118:119], v[126:127]
	v_add_f32_e32 v172, 1.0, v172
	v_rcp_f32_e32 v172, v172
	v_lshlrev_b32_e32 v126, 16, v115
	v_and_b32_e32 v127, 0xffff0000, v115
	v_lshlrev_b32_e32 v114, 16, v116
	v_and_b32_e32 v115, 0xffff0000, v116
	v_lshlrev_b32_e32 v132, 16, v117
	v_and_b32_e32 v133, 0xffff0000, v117
	s_waitcnt vmcnt(12)
	v_lshlrev_b32_e32 v116, 16, v110
	v_and_b32_e32 v117, 0xffff0000, v110
	v_pk_fma_f32 v[154:155], v[8:9], v[116:117], v[154:155]
	v_mul_f32_e32 v130, v130, v172
	v_mul_f32_e32 v154, v154, v130
	v_mul_f32_e32 v130, 0x3d372713, v131
	v_mul_f32_e32 v130, v131, v130
	v_fma_f32 v130, v131, v130, v131
	v_mul_f32_e32 v130, 0x3f4c422a, v130
	v_mul_f32_e32 v130, -2.0, v130
	v_mul_f32_e32 v130, 0x3fb8aa3b, v130
	v_exp_f32_e32 v130, v130
	v_pk_fma_f32 v[158:159], v[14:15], v[126:127], v[158:159]
	v_pk_fma_f32 v[160:161], v[22:23], v[162:163], v[152:153]
	v_lshlrev_b32_e32 v152, 16, v111
	v_add_f32_e32 v130, 1.0, v130
	v_rcp_f32_e32 v130, v130
	v_and_b32_e32 v153, 0xffff0000, v111
	v_pk_fma_f32 v[168:169], v[10:11], v[152:153], v[168:169]
	v_pk_fma_f32 v[148:149], v[4:5], v[114:115], v[148:149]
	v_mul_f32_e32 v130, v131, v130
	v_mul_f32_e32 v131, v155, v130
	v_mul_f32_e32 v130, 0x3d372713, v158
	v_mul_f32_e32 v130, v158, v130
	v_fma_f32 v130, v158, v130, v158
	v_mul_f32_e32 v130, 0x3f4c422a, v130
	v_mul_f32_e32 v130, -2.0, v130
	v_mul_f32_e32 v130, 0x3fb8aa3b, v130
	v_exp_f32_e32 v130, v130
	v_lshlrev_b32_e32 v110, 16, v112
	v_and_b32_e32 v111, 0xffff0000, v112
	v_pk_fma_f32 v[156:157], v[0:1], v[110:111], v[156:157]
	v_add_f32_e32 v130, 1.0, v130
	v_rcp_f32_e32 v130, v130
	v_pk_fma_f32 v[160:161], v[6:7], v[132:133], v[160:161]
	v_lshlrev_b32_e32 v112, 16, v113
	v_and_b32_e32 v113, 0xffff0000, v113
	v_mul_f32_e32 v130, v158, v130
	v_mul_f32_e32 v155, v168, v130
	v_mul_f32_e32 v130, 0x3d372713, v159
	v_mul_f32_e32 v130, v159, v130
	v_fma_f32 v130, v159, v130, v159
	v_mul_f32_e32 v130, 0x3f4c422a, v130
	v_mul_f32_e32 v130, -2.0, v130
	v_mul_f32_e32 v130, 0x3fb8aa3b, v130
	v_exp_f32_e32 v130, v130
	v_pk_fma_f32 v[170:171], v[2:3], v[112:113], v[170:171]
	v_pk_fma_f32 v[128:129], v[58:59], v[128:129], v[66:67]
	v_pk_fma_f32 v[118:119], v[24:25], v[118:119], v[42:43]
	v_add_f32_e32 v130, 1.0, v130
	v_rcp_f32_e32 v130, v130
	v_pk_fma_f32 v[124:125], v[46:47], v[124:125], v[50:51]
	v_pk_fma_f32 v[122:123], v[54:55], v[122:123], v[62:63]
	v_mul_f32_e32 v130, v159, v130
	v_mul_f32_e32 v158, v169, v130
	v_mul_f32_e32 v130, 0x3d372713, v148
	v_mul_f32_e32 v130, v148, v130
	v_fma_f32 v130, v148, v130, v148
	v_mul_f32_e32 v130, 0x3f4c422a, v130
	v_mul_f32_e32 v130, -2.0, v130
	v_mul_f32_e32 v130, 0x3fb8aa3b, v130
	v_exp_f32_e32 v130, v130
	s_nop 0
	v_add_f32_e32 v130, 1.0, v130
	v_rcp_f32_e32 v130, v130
	s_nop 0
	v_mul_f32_e32 v130, v148, v130
	v_mul_f32_e32 v148, v156, v130
	v_mul_f32_e32 v130, 0x3d372713, v149
	v_mul_f32_e32 v130, v149, v130
	v_fma_f32 v130, v149, v130, v149
	v_mul_f32_e32 v130, 0x3f4c422a, v130
	v_mul_f32_e32 v130, -2.0, v130
	v_mul_f32_e32 v130, 0x3fb8aa3b, v130
	v_exp_f32_e32 v130, v130
	s_nop 0
	v_add_f32_e32 v130, 1.0, v130
	v_rcp_f32_e32 v130, v130
	s_nop 0
	v_mul_f32_e32 v130, v149, v130
	v_mul_f32_e32 v149, v157, v130
	v_mul_f32_e32 v130, 0x3d372713, v160
	v_mul_f32_e32 v130, v160, v130
	v_fma_f32 v130, v160, v130, v160
	v_mul_f32_e32 v130, 0x3f4c422a, v130
	v_mul_f32_e32 v130, -2.0, v130
	v_mul_f32_e32 v130, 0x3fb8aa3b, v130
	v_exp_f32_e32 v130, v130
	s_nop 0
	v_add_f32_e32 v130, 1.0, v130
	v_rcp_f32_e32 v130, v130
	s_nop 0
	v_mul_f32_e32 v130, v160, v130
	v_mul_f32_e32 v156, v170, v130
	v_mul_f32_e32 v130, 0x3d372713, v161
	v_mul_f32_e32 v130, v161, v130
	v_fma_f32 v130, v161, v130, v161
	v_mul_f32_e32 v130, 0x3f4c422a, v130
	v_mul_f32_e32 v130, -2.0, v130
	v_mul_f32_e32 v130, 0x3fb8aa3b, v130
	v_exp_f32_e32 v130, v130
	s_nop 0
	v_add_f32_e32 v130, 1.0, v130
	v_rcp_f32_e32 v130, v130
	s_nop 0
	v_mul_f32_e32 v130, v161, v130
	v_mul_f32_e32 v157, v171, v130
	v_mov_b32_e32 v130, v33
	v_cvt_pk_fp8_f32 v130, v154, v131
	v_mov_b32_e32 v131, v33
	v_cvt_pk_fp8_f32 v131, v148, v149
	v_pk_fma_f32 v[160:161], v[16:17], v[110:111], v[118:119]
	v_cvt_pk_fp8_f32 v130, v155, v158 op_sel:[0,0,1]
	v_pk_fma_f32 v[154:155], v[38:39], v[120:121], v[128:129]
	v_cvt_pk_fp8_f32 v131, v156, v157 op_sel:[0,0,1]
	s_waitcnt vmcnt(11)
	v_lshlrev_b32_e32 v118, 16, v106
	v_and_b32_e32 v119, 0xffff0000, v106
	v_pk_fma_f32 v[148:149], v[48:49], v[164:165], v[52:53]
	global_store_dwordx2 v[146:147], v[130:131], off
	v_pk_fma_f32 v[130:131], v[60:61], v[150:151], v[68:69]
	v_pk_fma_f32 v[146:147], v[56:57], v[162:163], v[64:65]
	v_pk_fma_f32 v[150:151], v[26:27], v[166:167], v[44:45]
	v_pk_fma_f32 v[162:163], v[40:41], v[126:127], v[130:131]
	v_pk_fma_f32 v[164:165], v[22:23], v[132:133], v[146:147]
	v_pk_fma_f32 v[158:159], v[28:29], v[116:117], v[124:125]
	v_pk_fma_f32 v[168:169], v[18:19], v[112:113], v[150:151]
	v_lshlrev_b32_e32 v124, 16, v107
	v_and_b32_e32 v125, 0xffff0000, v107
	s_waitcnt vmcnt(11)
	v_lshlrev_b32_e32 v146, 16, v104
	v_and_b32_e32 v147, 0xffff0000, v104
	v_lshlrev_b32_e32 v150, 16, v105
	v_and_b32_e32 v151, 0xffff0000, v105
	v_pk_fma_f32 v[104:105], v[12:13], v[118:119], v[154:155]
	v_pk_fma_f32 v[166:167], v[30:31], v[152:153], v[148:149]
	v_lshlrev_b32_e32 v128, 16, v102
	v_and_b32_e32 v129, 0xffff0000, v102
	v_lshlrev_b32_e32 v148, 16, v103
	v_and_b32_e32 v149, 0xffff0000, v103
	v_pk_fma_f32 v[102:103], v[14:15], v[124:125], v[162:163]
	v_mul_f32_e32 v162, 0x3d372713, v104
	v_mul_f32_e32 v162, v104, v162
	v_fma_f32 v162, v104, v162, v104
	v_mul_f32_e32 v162, 0x3f4c422a, v162
	v_mul_f32_e32 v162, -2.0, v162
	v_mul_f32_e32 v162, 0x3fb8aa3b, v162
	v_exp_f32_e32 v162, v162
	v_pk_fma_f32 v[156:157], v[20:21], v[114:115], v[122:123]
	v_lshlrev_b32_e32 v122, 16, v108
	v_and_b32_e32 v123, 0xffff0000, v108
	v_add_f32_e32 v162, 1.0, v162
	v_rcp_f32_e32 v162, v162
	v_lshlrev_b32_e32 v130, 16, v109
	v_and_b32_e32 v131, 0xffff0000, v109
	v_pk_fma_f32 v[108:109], v[4:5], v[122:123], v[156:157]
	v_pk_fma_f32 v[156:157], v[8:9], v[128:129], v[158:159]
	v_mul_f32_e32 v104, v104, v162
	v_mul_f32_e32 v104, v156, v104
	v_mul_f32_e32 v156, 0x3d372713, v105
	v_mul_f32_e32 v156, v105, v156
	v_fma_f32 v156, v105, v156, v105
	v_mul_f32_e32 v156, 0x3f4c422a, v156
	v_mul_f32_e32 v156, -2.0, v156
	v_mul_f32_e32 v156, 0x3fb8aa3b, v156
	v_exp_f32_e32 v156, v156
	v_pk_fma_f32 v[154:155], v[10:11], v[148:149], v[166:167]
	v_pk_fma_f32 v[160:161], v[0:1], v[146:147], v[160:161]
	v_pk_fma_f32 v[106:107], v[6:7], v[130:131], v[164:165]
	v_add_f32_e32 v156, 1.0, v156
	v_rcp_f32_e32 v156, v156
	v_pk_fma_f32 v[158:159], v[2:3], v[150:151], v[168:169]
	v_pk_fma_f32 v[116:117], v[46:47], v[116:117], v[50:51]
	v_pk_fma_f32 v[112:113], v[26:27], v[112:113], v[44:45]
	v_mul_f32_e32 v105, v105, v156
	v_mul_f32_e32 v156, 0x3d372713, v102
	v_mul_f32_e32 v156, v102, v156
	v_fma_f32 v156, v102, v156, v102
	v_mul_f32_e32 v156, 0x3f4c422a, v156
	v_mul_f32_e32 v156, -2.0, v156
	v_mul_f32_e32 v156, 0x3fb8aa3b, v156
	v_exp_f32_e32 v156, v156
	v_mul_f32_e32 v105, v157, v105
	v_pk_fma_f32 v[110:111], v[24:25], v[110:111], v[42:43]
	v_add_f32_e32 v156, 1.0, v156
	v_rcp_f32_e32 v156, v156
	s_nop 0
	v_mul_f32_e32 v102, v102, v156
	v_mul_f32_e32 v154, v154, v102
	v_mul_f32_e32 v102, 0x3d372713, v103
	v_mul_f32_e32 v102, v103, v102
	v_fma_f32 v102, v103, v102, v103
	v_mul_f32_e32 v102, 0x3f4c422a, v102
	v_mul_f32_e32 v102, -2.0, v102
	v_mul_f32_e32 v102, 0x3fb8aa3b, v102
	v_exp_f32_e32 v102, v102
	s_nop 0
	v_add_f32_e32 v102, 1.0, v102
	v_rcp_f32_e32 v102, v102
	s_nop 0
	v_mul_f32_e32 v102, v103, v102
	v_mul_f32_e32 v103, v155, v102
	v_mul_f32_e32 v102, 0x3d372713, v108
	v_mul_f32_e32 v102, v108, v102
	v_fma_f32 v102, v108, v102, v108
	v_mul_f32_e32 v102, 0x3f4c422a, v102
	v_mul_f32_e32 v102, -2.0, v102
	v_mul_f32_e32 v102, 0x3fb8aa3b, v102
	v_exp_f32_e32 v102, v102
	s_nop 0
	v_add_f32_e32 v102, 1.0, v102
	v_rcp_f32_e32 v102, v102
	s_nop 0
	v_mul_f32_e32 v102, v108, v102
	v_mul_f32_e32 v108, v160, v102
	v_mul_f32_e32 v102, 0x3d372713, v109
	v_mul_f32_e32 v102, v109, v102
	v_fma_f32 v102, v109, v102, v109
	v_mul_f32_e32 v102, 0x3f4c422a, v102
	v_mul_f32_e32 v102, -2.0, v102
	v_mul_f32_e32 v102, 0x3fb8aa3b, v102
	v_exp_f32_e32 v102, v102
	s_nop 0
	v_add_f32_e32 v102, 1.0, v102
	v_rcp_f32_e32 v102, v102
	s_nop 0
	v_mul_f32_e32 v102, v109, v102
	v_mul_f32_e32 v109, v161, v102
	v_mul_f32_e32 v102, 0x3d372713, v106
	v_mul_f32_e32 v102, v106, v102
	v_fma_f32 v102, v106, v102, v106
	v_mul_f32_e32 v102, 0x3f4c422a, v102
	v_mul_f32_e32 v102, -2.0, v102
	v_mul_f32_e32 v102, 0x3fb8aa3b, v102
	v_exp_f32_e32 v102, v102
	s_nop 0
	v_add_f32_e32 v102, 1.0, v102
	v_rcp_f32_e32 v102, v102
	s_nop 0
	v_mul_f32_e32 v102, v106, v102
	v_mul_f32_e32 v106, v158, v102
	v_mul_f32_e32 v102, 0x3d372713, v107
	v_mul_f32_e32 v102, v107, v102
	v_fma_f32 v102, v107, v102, v107
	v_mul_f32_e32 v102, 0x3f4c422a, v102
	v_mul_f32_e32 v102, -2.0, v102
	v_mul_f32_e32 v102, 0x3fb8aa3b, v102
	v_exp_f32_e32 v102, v102
	s_nop 0
	v_add_f32_e32 v102, 1.0, v102
	v_rcp_f32_e32 v102, v102
	s_nop 0
	v_mul_f32_e32 v102, v107, v102
	v_mul_f32_e32 v107, v159, v102
	v_mov_b32_e32 v102, v33
	v_cvt_pk_fp8_f32 v102, v104, v105
	v_lshlrev_b64 v[104:105], 12, v[144:145]
	v_lshl_add_u64 v[104:105], v[134:135], 0, v[104:105]
	v_pk_fma_f32 v[158:159], v[18:19], v[150:151], v[112:113]
	v_cvt_pk_fp8_f32 v102, v154, v103 op_sel:[0,0,1]
	v_mov_b32_e32 v103, v33
	v_cvt_pk_fp8_f32 v103, v108, v109
	v_pk_fma_f32 v[108:109], v[54:55], v[114:115], v[62:63]
	v_pk_fma_f32 v[114:115], v[48:49], v[152:153], v[52:53]
	s_waitcnt vmcnt(9)
	v_lshlrev_b32_e32 v112, 16, v96
	v_cvt_pk_fp8_f32 v103, v106, v107 op_sel:[0,0,1]
	v_pk_fma_f32 v[106:107], v[56:57], v[132:133], v[64:65]
	v_pk_fma_f32 v[132:133], v[28:29], v[128:129], v[116:117]
	v_pk_fma_f32 v[154:155], v[22:23], v[130:131], v[106:107]
	global_store_dwordx2 v[104:105], v[102:103], off
	v_pk_fma_f32 v[102:103], v[60:61], v[126:127], v[68:69]
	v_pk_fma_f32 v[104:105], v[58:59], v[120:121], v[66:67]
	v_pk_fma_f32 v[152:153], v[40:41], v[124:125], v[102:103]
	v_pk_fma_f32 v[120:121], v[38:39], v[118:119], v[104:105]
	v_lshlrev_b32_e32 v102, 16, v98
	v_and_b32_e32 v103, 0xffff0000, v98
	v_lshlrev_b32_e32 v106, 16, v99
	v_and_b32_e32 v107, 0xffff0000, v99
	v_and_b32_e32 v113, 0xffff0000, v96
	v_lshlrev_b32_e32 v116, 16, v97
	v_and_b32_e32 v117, 0xffff0000, v97
	v_pk_fma_f32 v[96:97], v[12:13], v[102:103], v[120:121]
	v_pk_fma_f32 v[126:127], v[20:21], v[122:123], v[108:109]
	v_pk_fma_f32 v[156:157], v[30:31], v[148:149], v[114:115]
	v_lshlrev_b32_e32 v108, 16, v94
	v_and_b32_e32 v109, 0xffff0000, v94
	v_lshlrev_b32_e32 v114, 16, v95
	v_and_b32_e32 v115, 0xffff0000, v95
	v_pk_fma_f32 v[94:95], v[14:15], v[106:107], v[152:153]
	v_mul_f32_e32 v152, 0x3d372713, v96
	v_mul_f32_e32 v152, v96, v152
	v_fma_f32 v152, v96, v152, v96
	v_mul_f32_e32 v152, 0x3f4c422a, v152
	v_mul_f32_e32 v152, -2.0, v152
	v_mul_f32_e32 v152, 0x3fb8aa3b, v152
	v_exp_f32_e32 v152, v152
	v_lshlrev_b32_e32 v104, 16, v100
	v_and_b32_e32 v105, 0xffff0000, v100
	v_pk_fma_f32 v[144:145], v[16:17], v[146:147], v[110:111]
	v_add_f32_e32 v152, 1.0, v152
	v_rcp_f32_e32 v152, v152
	v_lshlrev_b32_e32 v110, 16, v101
	v_and_b32_e32 v111, 0xffff0000, v101
	v_pk_fma_f32 v[100:101], v[4:5], v[104:105], v[126:127]
	v_pk_fma_f32 v[126:127], v[8:9], v[108:109], v[132:133]
	v_mul_f32_e32 v96, v96, v152
	v_mul_f32_e32 v96, v126, v96
	v_mul_f32_e32 v126, 0x3d372713, v97
	v_mul_f32_e32 v126, v97, v126
	v_fma_f32 v126, v97, v126, v97
	v_mul_f32_e32 v126, 0x3f4c422a, v126
	v_mul_f32_e32 v126, -2.0, v126
	v_mul_f32_e32 v126, 0x3fb8aa3b, v126
	v_exp_f32_e32 v126, v126
	v_pk_fma_f32 v[120:121], v[10:11], v[114:115], v[156:157]
	v_pk_fma_f32 v[144:145], v[0:1], v[112:113], v[144:145]
	v_pk_fma_f32 v[98:99], v[6:7], v[110:111], v[154:155]
	v_add_f32_e32 v126, 1.0, v126
	v_rcp_f32_e32 v126, v126
	v_pk_fma_f32 v[132:133], v[2:3], v[116:117], v[158:159]
	v_mul_f32_e32 v97, v97, v126
	v_mul_f32_e32 v126, 0x3d372713, v94
	v_mul_f32_e32 v126, v94, v126
	v_fma_f32 v126, v94, v126, v94
	v_mul_f32_e32 v126, 0x3f4c422a, v126
	v_mul_f32_e32 v126, -2.0, v126
	v_mul_f32_e32 v126, 0x3fb8aa3b, v126
	v_exp_f32_e32 v126, v126
	v_mul_f32_e32 v97, v127, v97
	v_add_f32_e32 v126, 1.0, v126
	v_rcp_f32_e32 v126, v126
	s_nop 0
	v_mul_f32_e32 v94, v94, v126
	v_mul_f32_e32 v120, v120, v94
	v_mul_f32_e32 v94, 0x3d372713, v95
	v_mul_f32_e32 v94, v95, v94
	v_fma_f32 v94, v95, v94, v95
	v_mul_f32_e32 v94, 0x3f4c422a, v94
	v_mul_f32_e32 v94, -2.0, v94
	v_mul_f32_e32 v94, 0x3fb8aa3b, v94
	v_exp_f32_e32 v94, v94
	s_nop 0
	v_add_f32_e32 v94, 1.0, v94
	v_rcp_f32_e32 v94, v94
	s_nop 0
	v_mul_f32_e32 v94, v95, v94
	v_mul_f32_e32 v95, v121, v94
	v_mul_f32_e32 v94, 0x3d372713, v100
	v_mul_f32_e32 v94, v100, v94
	v_fma_f32 v94, v100, v94, v100
	v_mul_f32_e32 v94, 0x3f4c422a, v94
	v_mul_f32_e32 v94, -2.0, v94
	v_mul_f32_e32 v94, 0x3fb8aa3b, v94
	v_exp_f32_e32 v94, v94
	s_nop 0
	v_add_f32_e32 v94, 1.0, v94
	v_rcp_f32_e32 v94, v94
	s_nop 0
	v_mul_f32_e32 v94, v100, v94
	v_mul_f32_e32 v100, v144, v94
	v_mul_f32_e32 v94, 0x3d372713, v101
	v_mul_f32_e32 v94, v101, v94
	v_fma_f32 v94, v101, v94, v101
	v_mul_f32_e32 v94, 0x3f4c422a, v94
	v_mul_f32_e32 v94, -2.0, v94
	v_mul_f32_e32 v94, 0x3fb8aa3b, v94
	v_exp_f32_e32 v94, v94
	s_nop 0
	v_add_f32_e32 v94, 1.0, v94
	v_rcp_f32_e32 v94, v94
	s_nop 0
	v_mul_f32_e32 v94, v101, v94
	v_mul_f32_e32 v101, v145, v94
	v_mul_f32_e32 v94, 0x3d372713, v98
	v_mul_f32_e32 v94, v98, v94
	v_fma_f32 v94, v98, v94, v98
	v_mul_f32_e32 v94, 0x3f4c422a, v94
	v_mul_f32_e32 v94, -2.0, v94
	v_mul_f32_e32 v94, 0x3fb8aa3b, v94
	v_exp_f32_e32 v94, v94
	s_nop 0
	v_add_f32_e32 v94, 1.0, v94
	v_rcp_f32_e32 v94, v94
	s_nop 0
	v_mul_f32_e32 v94, v98, v94
	v_mul_f32_e32 v98, v132, v94
	v_mul_f32_e32 v94, 0x3d372713, v99
	v_mul_f32_e32 v94, v99, v94
	v_fma_f32 v94, v99, v94, v99
	v_mul_f32_e32 v94, 0x3f4c422a, v94
	v_mul_f32_e32 v94, -2.0, v94
	v_mul_f32_e32 v94, 0x3fb8aa3b, v94
	v_exp_f32_e32 v94, v94
	s_nop 0
	v_add_f32_e32 v94, 1.0, v94
	v_rcp_f32_e32 v94, v94
	s_nop 0
	v_mul_f32_e32 v94, v99, v94
	v_mul_f32_e32 v99, v133, v94
	v_mov_b32_e32 v94, v33
	v_cvt_pk_fp8_f32 v94, v96, v97
	v_lshlrev_b64 v[96:97], 12, v[142:143]
	v_lshl_add_u64 v[96:97], v[134:135], 0, v[96:97]
	v_pk_fma_f32 v[142:143], v[24:25], v[146:147], v[42:43]
	v_cvt_pk_fp8_f32 v94, v120, v95 op_sel:[0,0,1]
	v_mov_b32_e32 v95, v33
	v_cvt_pk_fp8_f32 v95, v100, v101
	v_pk_fma_f32 v[100:101], v[54:55], v[122:123], v[62:63]
	v_pk_fma_f32 v[122:123], v[46:47], v[128:129], v[50:51]
	v_pk_fma_f32 v[120:121], v[20:21], v[104:105], v[100:101]
	v_cvt_pk_fp8_f32 v95, v98, v99 op_sel:[0,0,1]
	v_pk_fma_f32 v[98:99], v[56:57], v[130:131], v[64:65]
	v_pk_fma_f32 v[122:123], v[28:29], v[108:109], v[122:123]
	v_pk_fma_f32 v[128:129], v[22:23], v[110:111], v[98:99]
	global_store_dwordx2 v[96:97], v[94:95], off
	v_pk_fma_f32 v[94:95], v[60:61], v[124:125], v[68:69]
	v_pk_fma_f32 v[96:97], v[58:59], v[118:119], v[66:67]
	v_pk_fma_f32 v[126:127], v[40:41], v[106:107], v[94:95]
	v_pk_fma_f32 v[118:119], v[38:39], v[102:103], v[96:97]
	s_waitcnt vmcnt(10)
	v_lshlrev_b32_e32 v94, 16, v90
	v_and_b32_e32 v95, 0xffff0000, v90
	v_pk_fma_f32 v[124:125], v[48:49], v[148:149], v[52:53]
	v_pk_fma_f32 v[118:119], v[12:13], v[94:95], v[118:119]
	v_pk_fma_f32 v[130:131], v[30:31], v[114:115], v[124:125]
	v_pk_fma_f32 v[124:125], v[16:17], v[112:113], v[142:143]
	v_mul_f32_e32 v142, 0x3d372713, v118
	v_mul_f32_e32 v142, v118, v142
	v_fma_f32 v142, v118, v142, v118
	v_mul_f32_e32 v142, 0x3f4c422a, v142
	v_mul_f32_e32 v142, -2.0, v142
	v_mul_f32_e32 v142, 0x3fb8aa3b, v142
	v_exp_f32_e32 v142, v142
	v_lshlrev_b32_e32 v98, 16, v91
	v_and_b32_e32 v99, 0xffff0000, v91
	s_waitcnt vmcnt(9)
	v_lshlrev_b32_e32 v90, 16, v86
	v_add_f32_e32 v142, 1.0, v142
	v_rcp_f32_e32 v142, v142
	v_and_b32_e32 v91, 0xffff0000, v86
	v_pk_fma_f32 v[122:123], v[8:9], v[90:91], v[122:123]
	v_pk_fma_f32 v[126:127], v[14:15], v[98:99], v[126:127]
	v_mul_f32_e32 v118, v118, v142
	v_mul_f32_e32 v122, v122, v118
	v_mul_f32_e32 v118, 0x3d372713, v119
	v_mul_f32_e32 v118, v119, v118
	v_fma_f32 v118, v119, v118, v119
	v_mul_f32_e32 v118, 0x3f4c422a, v118
	v_mul_f32_e32 v118, -2.0, v118
	v_mul_f32_e32 v118, 0x3fb8aa3b, v118
	v_exp_f32_e32 v118, v118
	v_lshlrev_b32_e32 v96, 16, v92
	v_and_b32_e32 v97, 0xffff0000, v92
	v_lshlrev_b32_e32 v100, 16, v93
	v_add_f32_e32 v118, 1.0, v118
	v_rcp_f32_e32 v118, v118
	v_and_b32_e32 v101, 0xffff0000, v93
	v_lshlrev_b32_e32 v92, 16, v87
	v_and_b32_e32 v93, 0xffff0000, v87
	v_mul_f32_e32 v118, v119, v118
	v_mul_f32_e32 v119, v123, v118
	v_mul_f32_e32 v118, 0x3d372713, v126
	v_mul_f32_e32 v118, v126, v118
	v_fma_f32 v118, v126, v118, v126
	v_mul_f32_e32 v118, 0x3f4c422a, v118
	v_mul_f32_e32 v118, -2.0, v118
	v_mul_f32_e32 v118, 0x3fb8aa3b, v118
	v_exp_f32_e32 v118, v118
	v_pk_fma_f32 v[130:131], v[10:11], v[92:93], v[130:131]
	v_pk_fma_f32 v[120:121], v[4:5], v[96:97], v[120:121]
	v_lshlrev_b32_e32 v86, 16, v88
	v_add_f32_e32 v118, 1.0, v118
	v_rcp_f32_e32 v118, v118
	v_and_b32_e32 v87, 0xffff0000, v88
	v_pk_fma_f32 v[124:125], v[0:1], v[86:87], v[124:125]
	v_pk_fma_f32 v[128:129], v[6:7], v[100:101], v[128:129]
	v_mul_f32_e32 v118, v126, v118
	v_mul_f32_e32 v123, v130, v118
	v_mul_f32_e32 v118, 0x3d372713, v127
	v_mul_f32_e32 v118, v127, v118
	v_fma_f32 v118, v127, v118, v127
	v_mul_f32_e32 v118, 0x3f4c422a, v118
	v_mul_f32_e32 v118, -2.0, v118
	v_mul_f32_e32 v118, 0x3fb8aa3b, v118
	v_exp_f32_e32 v118, v118
	v_pk_fma_f32 v[132:133], v[26:27], v[150:151], v[44:45]
	v_lshlrev_b32_e32 v88, 16, v89
	v_pk_fma_f32 v[132:133], v[18:19], v[116:117], v[132:133]
	v_add_f32_e32 v118, 1.0, v118
	v_rcp_f32_e32 v118, v118
	v_and_b32_e32 v89, 0xffff0000, v89
	v_pk_fma_f32 v[132:133], v[2:3], v[88:89], v[132:133]
	v_pk_fma_f32 v[102:103], v[58:59], v[102:103], v[66:67]
	v_mul_f32_e32 v118, v127, v118
	v_mul_f32_e32 v126, v131, v118
	v_mul_f32_e32 v118, 0x3d372713, v120
	v_mul_f32_e32 v118, v120, v118
	v_fma_f32 v118, v120, v118, v120
	v_mul_f32_e32 v118, 0x3f4c422a, v118
	v_mul_f32_e32 v118, -2.0, v118
	v_mul_f32_e32 v118, 0x3fb8aa3b, v118
	v_exp_f32_e32 v118, v118
	v_pk_fma_f32 v[108:109], v[46:47], v[108:109], v[50:51]
	v_pk_fma_f32 v[112:113], v[24:25], v[112:113], v[42:43]
	v_pk_fma_f32 v[58:59], v[58:59], v[94:95], v[66:67]
	v_add_f32_e32 v118, 1.0, v118
	v_rcp_f32_e32 v118, v118
	v_pk_fma_f32 v[24:25], v[24:25], v[86:87], v[42:43]
	v_pk_fma_f32 v[112:113], v[16:17], v[86:87], v[112:113]
	v_pk_fma_f32 v[46:47], v[46:47], v[90:91], v[50:51]
	v_mul_f32_e32 v118, v120, v118
	v_mul_f32_e32 v120, v124, v118
	v_mul_f32_e32 v118, 0x3d372713, v121
	v_mul_f32_e32 v118, v121, v118
	v_fma_f32 v118, v121, v118, v121
	v_mul_f32_e32 v118, 0x3f4c422a, v118
	v_mul_f32_e32 v118, -2.0, v118
	v_mul_f32_e32 v118, 0x3fb8aa3b, v118
	v_exp_f32_e32 v118, v118
	s_waitcnt vmcnt(6)
	v_lshlrev_b32_e32 v50, 16, v72
	v_and_b32_e32 v51, 0xffff0000, v72
	v_pk_fma_f32 v[106:107], v[60:61], v[106:107], v[68:69]
	v_add_f32_e32 v118, 1.0, v118
	v_rcp_f32_e32 v118, v118
	v_pk_fma_f32 v[116:117], v[26:27], v[116:117], v[44:45]
	v_pk_fma_f32 v[60:61], v[60:61], v[98:99], v[68:69]
	v_pk_fma_f32 v[26:27], v[26:27], v[88:89], v[44:45]
	v_mul_f32_e32 v118, v121, v118
	v_mul_f32_e32 v121, v125, v118
	v_mul_f32_e32 v118, 0x3d372713, v128
	v_mul_f32_e32 v118, v128, v118
	v_fma_f32 v118, v128, v118, v128
	v_mul_f32_e32 v118, 0x3f4c422a, v118
	v_mul_f32_e32 v118, -2.0, v118
	v_mul_f32_e32 v118, 0x3fb8aa3b, v118
	v_exp_f32_e32 v118, v118
	v_pk_fma_f32 v[116:117], v[18:19], v[88:89], v[116:117]
	v_pk_fma_f32 v[114:115], v[48:49], v[114:115], v[52:53]
	v_pk_fma_f32 v[48:49], v[48:49], v[92:93], v[52:53]
	v_add_f32_e32 v118, 1.0, v118
	v_rcp_f32_e32 v118, v118
	v_pk_fma_f32 v[114:115], v[30:31], v[92:93], v[114:115]
	v_pk_fma_f32 v[104:105], v[54:55], v[104:105], v[62:63]
	v_pk_fma_f32 v[54:55], v[54:55], v[96:97], v[62:63]
	v_mul_f32_e32 v118, v128, v118
	v_mul_f32_e32 v124, v132, v118
	v_mul_f32_e32 v118, 0x3d372713, v129
	v_mul_f32_e32 v118, v129, v118
	v_fma_f32 v118, v129, v118, v129
	v_mul_f32_e32 v118, 0x3f4c422a, v118
	v_mul_f32_e32 v118, -2.0, v118
	v_mul_f32_e32 v118, 0x3fb8aa3b, v118
	v_exp_f32_e32 v118, v118
	s_waitcnt vmcnt(5)
	v_lshlrev_b32_e32 v42, 16, v76
	v_and_b32_e32 v43, 0xffff0000, v76
	v_pk_fma_f32 v[110:111], v[56:57], v[110:111], v[64:65]
	v_add_f32_e32 v118, 1.0, v118
	v_rcp_f32_e32 v118, v118
	v_pk_fma_f32 v[56:57], v[56:57], v[100:101], v[64:65]
	v_pk_fma_f32 v[110:111], v[22:23], v[100:101], v[110:111]
	v_lshlrev_b32_e32 v44, 16, v77
	v_mul_f32_e32 v118, v129, v118
	v_mul_f32_e32 v125, v133, v118
	v_mov_b32_e32 v118, v33
	v_cvt_pk_fp8_f32 v118, v122, v119
	v_mov_b32_e32 v119, v33
	v_cvt_pk_fp8_f32 v119, v120, v121
	v_lshlrev_b64 v[120:121], 12, v[140:141]
	v_cvt_pk_fp8_f32 v118, v123, v126 op_sel:[0,0,1]
	v_lshl_add_u64 v[120:121], v[134:135], 0, v[120:121]
	v_cvt_pk_fp8_f32 v119, v124, v125 op_sel:[0,0,1]
	v_pk_fma_f32 v[124:125], v[28:29], v[90:91], v[108:109]
	v_lshlrev_b32_e32 v108, 16, v80
	v_and_b32_e32 v109, 0xffff0000, v80
	global_store_dwordx2 v[120:121], v[118:119], off
	v_pk_fma_f32 v[118:119], v[38:39], v[94:95], v[102:103]
	v_lshlrev_b32_e32 v102, 16, v82
	v_and_b32_e32 v103, 0xffff0000, v82
	v_pk_fma_f32 v[38:39], v[38:39], v[102:103], v[58:59]
	v_pk_fma_f32 v[16:17], v[16:17], v[108:109], v[24:25]
	v_lshlrev_b32_e32 v24, 16, v74
	v_and_b32_e32 v25, 0xffff0000, v74
	v_pk_fma_f32 v[118:119], v[12:13], v[102:103], v[118:119]
	v_pk_fma_f32 v[12:13], v[12:13], v[24:25], v[38:39]
	v_pk_fma_f32 v[112:113], v[0:1], v[108:109], v[112:113]
	v_pk_fma_f32 v[0:1], v[0:1], v[50:51], v[16:17]
	v_mul_f32_e32 v16, 0x3d372713, v12
	v_mul_f32_e32 v126, 0x3d372713, v118
	v_mul_f32_e32 v16, v12, v16
	v_mul_f32_e32 v126, v118, v126
	v_fma_f32 v16, v12, v16, v12
	v_fma_f32 v126, v118, v126, v118
	v_mul_f32_e32 v16, 0x3f4c422a, v16
	v_mul_f32_e32 v126, 0x3f4c422a, v126
	v_mul_f32_e32 v16, -2.0, v16
	v_mul_f32_e32 v126, -2.0, v126
	v_mul_f32_e32 v16, 0x3fb8aa3b, v16
	v_mul_f32_e32 v126, 0x3fb8aa3b, v126
	v_exp_f32_e32 v16, v16
	v_exp_f32_e32 v126, v126
	v_pk_fma_f32 v[120:121], v[40:41], v[98:99], v[106:107]
	v_lshlrev_b32_e32 v106, 16, v78
	v_add_f32_e32 v16, 1.0, v16
	v_add_f32_e32 v126, 1.0, v126
	v_rcp_f32_e32 v16, v16
	v_rcp_f32_e32 v126, v126
	v_and_b32_e32 v107, 0xffff0000, v78
	v_pk_fma_f32 v[28:29], v[28:29], v[106:107], v[46:47]
	v_lshlrev_b32_e32 v46, 16, v70
	v_and_b32_e32 v47, 0xffff0000, v70
	v_pk_fma_f32 v[124:125], v[8:9], v[106:107], v[124:125]
	v_pk_fma_f32 v[8:9], v[8:9], v[46:47], v[28:29]
	v_mul_f32_e32 v12, v12, v16
	v_mul_f32_e32 v118, v118, v126
	v_mul_f32_e32 v8, v8, v12
	v_mul_f32_e32 v12, 0x3d372713, v13
	v_mul_f32_e32 v118, v124, v118
	v_mul_f32_e32 v124, 0x3d372713, v119
	v_mul_f32_e32 v12, v13, v12
	v_mul_f32_e32 v124, v119, v124
	v_fma_f32 v12, v13, v12, v13
	v_fma_f32 v124, v119, v124, v119
	v_mul_f32_e32 v12, 0x3f4c422a, v12
	v_mul_f32_e32 v124, 0x3f4c422a, v124
	v_mul_f32_e32 v12, -2.0, v12
	v_mul_f32_e32 v124, -2.0, v124
	v_mul_f32_e32 v12, 0x3fb8aa3b, v12
	v_mul_f32_e32 v124, 0x3fb8aa3b, v124
	v_exp_f32_e32 v12, v12
	v_exp_f32_e32 v124, v124
	v_lshlrev_b32_e32 v82, 16, v83
	v_and_b32_e32 v83, 0xffff0000, v83
	v_add_f32_e32 v12, 1.0, v12
	v_add_f32_e32 v124, 1.0, v124
	v_rcp_f32_e32 v12, v12
	v_rcp_f32_e32 v124, v124
	v_lshlrev_b32_e32 v80, 16, v81
	v_and_b32_e32 v81, 0xffff0000, v81
	v_pk_fma_f32 v[40:41], v[40:41], v[82:83], v[60:61]
	v_pk_fma_f32 v[18:19], v[18:19], v[80:81], v[26:27]
	v_lshlrev_b32_e32 v26, 16, v75
	v_and_b32_e32 v27, 0xffff0000, v75
	v_pk_fma_f32 v[120:121], v[14:15], v[82:83], v[120:121]
	v_pk_fma_f32 v[14:15], v[14:15], v[26:27], v[40:41]
	v_mul_f32_e32 v12, v13, v12
	v_mul_f32_e32 v119, v119, v124
	v_mul_f32_e32 v124, 0x3d372713, v120
	v_mul_f32_e32 v9, v9, v12
	v_mul_f32_e32 v12, 0x3d372713, v14
	v_mul_f32_e32 v124, v120, v124
	v_mul_f32_e32 v12, v14, v12
	v_fma_f32 v124, v120, v124, v120
	v_fma_f32 v12, v14, v12, v14
	v_mul_f32_e32 v124, 0x3f4c422a, v124
	v_mul_f32_e32 v12, 0x3f4c422a, v12
	v_mul_f32_e32 v124, -2.0, v124
	v_mul_f32_e32 v12, -2.0, v12
	v_mul_f32_e32 v124, 0x3fb8aa3b, v124
	v_mul_f32_e32 v12, 0x3fb8aa3b, v12
	v_exp_f32_e32 v124, v124
	v_exp_f32_e32 v12, v12
	v_lshlrev_b32_e32 v78, 16, v79
	v_and_b32_e32 v79, 0xffff0000, v79
	v_add_f32_e32 v124, 1.0, v124
	v_add_f32_e32 v12, 1.0, v12
	v_rcp_f32_e32 v124, v124
	v_rcp_f32_e32 v12, v12
	v_pk_fma_f32 v[30:31], v[30:31], v[78:79], v[48:49]
	v_lshlrev_b32_e32 v48, 16, v71
	v_and_b32_e32 v49, 0xffff0000, v71
	v_pk_fma_f32 v[114:115], v[10:11], v[78:79], v[114:115]
	v_mul_f32_e32 v120, v120, v124
	v_pk_fma_f32 v[10:11], v[10:11], v[48:49], v[30:31]
	v_mul_f32_e32 v12, v14, v12
	v_mul_f32_e32 v114, v114, v120
	v_mul_f32_e32 v120, 0x3d372713, v121
	v_mul_f32_e32 v10, v10, v12
	v_mul_f32_e32 v12, 0x3d372713, v15
	v_mul_f32_e32 v120, v121, v120
	v_mul_f32_e32 v12, v15, v12
	v_fma_f32 v120, v121, v120, v121
	v_fma_f32 v12, v15, v12, v15
	v_mul_f32_e32 v120, 0x3f4c422a, v120
	v_mul_f32_e32 v12, 0x3f4c422a, v12
	v_mul_f32_e32 v120, -2.0, v120
	v_mul_f32_e32 v12, -2.0, v12
	v_mul_f32_e32 v120, 0x3fb8aa3b, v120
	v_mul_f32_e32 v12, 0x3fb8aa3b, v12
	v_exp_f32_e32 v120, v120
	v_exp_f32_e32 v12, v12
	v_pk_fma_f32 v[122:123], v[20:21], v[96:97], v[104:105]
	v_lshlrev_b32_e32 v104, 16, v84
	v_add_f32_e32 v120, 1.0, v120
	v_add_f32_e32 v12, 1.0, v12
	v_rcp_f32_e32 v120, v120
	v_rcp_f32_e32 v12, v12
	v_and_b32_e32 v105, 0xffff0000, v84
	v_pk_fma_f32 v[20:21], v[20:21], v[104:105], v[54:55]
	v_pk_fma_f32 v[122:123], v[4:5], v[104:105], v[122:123]
	v_mul_f32_e32 v120, v121, v120
	v_pk_fma_f32 v[4:5], v[4:5], v[42:43], v[20:21]
	v_mul_f32_e32 v12, v15, v12
	v_mul_f32_e32 v115, v115, v120
	v_mul_f32_e32 v120, 0x3d372713, v122
	v_mul_f32_e32 v11, v11, v12
	v_mul_f32_e32 v12, 0x3d372713, v4
	v_mul_f32_e32 v120, v122, v120
	v_mul_f32_e32 v12, v4, v12
	v_fma_f32 v120, v122, v120, v122
	v_fma_f32 v12, v4, v12, v4
	v_mul_f32_e32 v120, 0x3f4c422a, v120
	v_mul_f32_e32 v12, 0x3f4c422a, v12
	v_mul_f32_e32 v120, -2.0, v120
	v_mul_f32_e32 v12, -2.0, v12
	v_mul_f32_e32 v120, 0x3fb8aa3b, v120
	v_mul_f32_e32 v12, 0x3fb8aa3b, v12
	v_exp_f32_e32 v120, v120
	v_exp_f32_e32 v12, v12
	v_lshlrev_b32_e32 v84, 16, v85
	v_and_b32_e32 v85, 0xffff0000, v85
	v_add_f32_e32 v120, 1.0, v120
	v_add_f32_e32 v12, 1.0, v12
	v_rcp_f32_e32 v120, v120
	v_rcp_f32_e32 v12, v12
	v_pk_fma_f32 v[22:23], v[22:23], v[84:85], v[56:57]
	v_and_b32_e32 v45, 0xffff0000, v77
	v_mul_f32_e32 v120, v122, v120
	v_mul_f32_e32 v4, v4, v12
	v_mul_f32_e32 v112, v112, v120
	v_mul_f32_e32 v120, 0x3d372713, v123
	v_mul_f32_e32 v4, v0, v4
	v_mul_f32_e32 v0, 0x3d372713, v5
	v_mul_f32_e32 v120, v123, v120
	v_mul_f32_e32 v0, v5, v0
	v_fma_f32 v120, v123, v120, v123
	v_fma_f32 v0, v5, v0, v5
	v_mul_f32_e32 v120, 0x3f4c422a, v120
	v_mul_f32_e32 v0, 0x3f4c422a, v0
	v_mul_f32_e32 v120, -2.0, v120
	v_mul_f32_e32 v0, -2.0, v0
	v_mul_f32_e32 v120, 0x3fb8aa3b, v120
	v_mul_f32_e32 v0, 0x3fb8aa3b, v0
	v_exp_f32_e32 v120, v120
	v_exp_f32_e32 v0, v0
	v_pk_fma_f32 v[110:111], v[6:7], v[84:85], v[110:111]
	v_pk_fma_f32 v[6:7], v[6:7], v[44:45], v[22:23]
	v_add_f32_e32 v120, 1.0, v120
	v_add_f32_e32 v0, 1.0, v0
	v_rcp_f32_e32 v120, v120
	v_rcp_f32_e32 v0, v0
	v_lshlrev_b32_e32 v52, 16, v73
	v_and_b32_e32 v53, 0xffff0000, v73
	v_mul_f32_e32 v120, v123, v120
	v_mul_f32_e32 v0, v5, v0
	v_mul_f32_e32 v113, v113, v120
	v_mul_f32_e32 v120, 0x3d372713, v110
	v_mul_f32_e32 v5, v1, v0
	v_mul_f32_e32 v0, 0x3d372713, v6
	v_mul_f32_e32 v120, v110, v120
	v_mul_f32_e32 v0, v6, v0
	v_fma_f32 v120, v110, v120, v110
	v_fma_f32 v0, v6, v0, v6
	v_mul_f32_e32 v120, 0x3f4c422a, v120
	v_mul_f32_e32 v0, 0x3f4c422a, v0
	v_mul_f32_e32 v120, -2.0, v120
	v_mul_f32_e32 v0, -2.0, v0
	v_mul_f32_e32 v120, 0x3fb8aa3b, v120
	v_mul_f32_e32 v0, 0x3fb8aa3b, v0
	v_exp_f32_e32 v120, v120
	v_exp_f32_e32 v0, v0
	v_pk_fma_f32 v[116:117], v[2:3], v[80:81], v[116:117]
	v_pk_fma_f32 v[2:3], v[2:3], v[52:53], v[18:19]
	v_add_f32_e32 v120, 1.0, v120
	v_add_f32_e32 v0, 1.0, v0
	v_rcp_f32_e32 v120, v120
	v_rcp_f32_e32 v0, v0
	v_mul_f32_e32 v119, v125, v119
	v_mov_b32_e32 v1, v33
	v_mul_f32_e32 v110, v110, v120
	v_mul_f32_e32 v0, v6, v0
	v_mul_f32_e32 v116, v116, v110
	v_mul_f32_e32 v110, 0x3d372713, v111
	v_mul_f32_e32 v2, v2, v0
	v_mul_f32_e32 v0, 0x3d372713, v7
	v_mul_f32_e32 v110, v111, v110
	v_mul_f32_e32 v0, v7, v0
	v_fma_f32 v110, v111, v110, v111
	v_fma_f32 v0, v7, v0, v7
	v_mul_f32_e32 v110, 0x3f4c422a, v110
	v_mul_f32_e32 v0, 0x3f4c422a, v0
	v_mul_f32_e32 v110, -2.0, v110
	v_mul_f32_e32 v0, -2.0, v0
	v_mul_f32_e32 v110, 0x3fb8aa3b, v110
	v_mul_f32_e32 v0, 0x3fb8aa3b, v0
	v_exp_f32_e32 v110, v110
	v_exp_f32_e32 v0, v0
	v_cvt_pk_fp8_f32 v1, v4, v5
	v_add_f32_e32 v110, 1.0, v110
	v_add_f32_e32 v0, 1.0, v0
	v_rcp_f32_e32 v110, v110
	v_rcp_f32_e32 v0, v0
	v_mul_f32_e32 v110, v111, v110
	v_mul_f32_e32 v0, v7, v0
	v_mul_f32_e32 v117, v117, v110
	v_mov_b32_e32 v110, v33
	v_mov_b32_e32 v111, v33
	v_mul_f32_e32 v3, v3, v0
	v_mov_b32_e32 v0, v33
	v_cvt_pk_fp8_f32 v110, v118, v119
	v_cvt_pk_fp8_f32 v111, v112, v113
	v_cvt_pk_fp8_f32 v0, v8, v9
	v_cvt_pk_fp8_f32 v1, v2, v3 op_sel:[0,0,1]
	v_cvt_pk_fp8_f32 v110, v114, v115 op_sel:[0,0,1]
	v_cvt_pk_fp8_f32 v111, v116, v117 op_sel:[0,0,1]
	v_cvt_pk_fp8_f32 v0, v10, v11 op_sel:[0,0,1]
	v_lshlrev_b64 v[112:113], 12, v[138:139]
	v_lshlrev_b64 v[2:3], 12, v[136:137]
	v_lshl_add_u64 v[112:113], v[134:135], 0, v[112:113]
	v_lshl_add_u64 v[2:3], v[134:135], 0, v[2:3]
	global_store_dwordx2 v[112:113], v[110:111], off
	global_store_dwordx2 v[2:3], v[0:1], off
	s_andn2_b64 exec, exec, s[24:25]
	s_cbranch_execnz .LBB0_1912
